# hot loop heads (GEMM K-loops, attention, scan, gMLP) aligned to 64 bytes with .p2align 6
# speedup vs baseline: 1.0020x; 1.0012x over previous
.Lpeel_inproj:
	s_add_u32 s28, s76, 0xfffc0080
	s_addc_u32 s29, s77, -1
	s_add_i32 s30, 0, 0x10000
	s_cmp_eq_u32 s71, 12
	s_cselect_b32 s83, s36, s29
	s_cselect_b32 s82, s37, s28
	v_add_u32_e32 v112, s30, v153
	s_cselect_b32 s81, s43, s65
	s_cselect_b32 s80, s50, s51
	s_add_i32 s31, 0, 0x14000
	ds_read_b128 v[130:133], v112
	ds_read_b128 v[134:137], v112 offset:1024
	ds_read_b128 v[156:159], v112 offset:2048
	ds_read_b128 v[160:163], v112 offset:3072
	v_add_u32_e32 v112, s31, v153
	ds_read_b128 v[164:167], v112
	ds_read_b128 v[168:171], v112 offset:1024
	ds_read_b128 v[172:175], v112 offset:2048
	ds_read_b128 v[176:179], v112 offset:3072
	v_lshl_add_u64 v[150:151], s[76:77], 0, v[146:147]
	s_add_i32 m0, s26, 0xc000
	ds_read_b128 v[180:183], v154
	ds_read_b128 v[184:187], v154 offset:1024
	ds_read_b128 v[188:191], v154 offset:2048
	ds_read_b128 v[192:195], v154 offset:3072
	ds_read_b128 v[206:209], v154 offset:4096
	ds_read_b128 v[210:213], v154 offset:5120
	ds_read_b128 v[216:219], v154 offset:6144
	ds_read_b128 v[220:223], v154 offset:7168
	global_load_lds_dwordx4 v[150:151], off
	v_lshl_add_u64 v[150:151], s[76:77], 0, v[148:149]
	s_add_i32 m0, s26, 0xe000
	s_nop 0
	global_load_lds_dwordx4 v[150:151], off
	s_waitcnt vmcnt(8)
	s_waitcnt lgkmcnt(0)
	s_barrier
	s_setprio 1
	s_waitcnt lgkmcnt(0)
	v_mfma_f32_16x16x32_bf16 v[126:129], v[130:133], v[180:183], 0
	v_mfma_f32_16x16x32_bf16 v[122:125], v[156:159], v[180:183], 0
	v_mfma_f32_16x16x32_bf16 v[118:121], v[130:133], v[188:191], 0
	v_mfma_f32_16x16x32_bf16 v[114:117], v[156:159], v[188:191], 0
	v_mfma_f32_16x16x32_bf16 v[100:103], v[130:133], v[206:209], 0
	v_mfma_f32_16x16x32_bf16 v[96:99], v[156:159], v[206:209], 0
	v_mfma_f32_16x16x32_bf16 v[84:87], v[130:133], v[216:219], 0
	v_mfma_f32_16x16x32_bf16 v[80:83], v[156:159], v[216:219], 0
	v_mfma_f32_16x16x32_bf16 v[126:129], v[134:137], v[184:187], v[126:129]
	v_mfma_f32_16x16x32_bf16 v[122:125], v[160:163], v[184:187], v[122:125]
	v_mfma_f32_16x16x32_bf16 v[118:121], v[134:137], v[192:195], v[118:121]
	v_mfma_f32_16x16x32_bf16 v[114:117], v[160:163], v[192:195], v[114:117]
	v_mfma_f32_16x16x32_bf16 v[100:103], v[134:137], v[210:213], v[100:103]
	v_mfma_f32_16x16x32_bf16 v[96:99], v[160:163], v[210:213], v[96:99]
	v_mfma_f32_16x16x32_bf16 v[84:87], v[134:137], v[220:223], v[84:87]
	v_mfma_f32_16x16x32_bf16 v[80:83], v[160:163], v[220:223], v[80:83]
	s_setprio 0
	s_setprio 1
	v_mfma_f32_16x16x32_bf16 v[108:111], v[164:167], v[180:183], 0
	v_mfma_f32_16x16x32_bf16 v[104:107], v[172:175], v[180:183], 0
	v_mfma_f32_16x16x32_bf16 v[92:95], v[164:167], v[188:191], 0
	v_mfma_f32_16x16x32_bf16 v[88:91], v[172:175], v[188:191], 0
	v_mfma_f32_16x16x32_bf16 v[76:79], v[164:167], v[206:209], 0
	v_mfma_f32_16x16x32_bf16 v[72:75], v[172:175], v[206:209], 0
	v_mfma_f32_16x16x32_bf16 v[68:71], v[164:167], v[216:219], 0
	v_mfma_f32_16x16x32_bf16 v[64:67], v[172:175], v[216:219], 0
	v_mfma_f32_16x16x32_bf16 v[108:111], v[168:171], v[184:187], v[108:111]
	v_mfma_f32_16x16x32_bf16 v[104:107], v[176:179], v[184:187], v[104:107]
	v_mfma_f32_16x16x32_bf16 v[92:95], v[168:171], v[192:195], v[92:95]
	v_mfma_f32_16x16x32_bf16 v[88:91], v[176:179], v[192:195], v[88:91]
	v_mfma_f32_16x16x32_bf16 v[76:79], v[168:171], v[210:213], v[76:79]
	v_mfma_f32_16x16x32_bf16 v[72:75], v[176:179], v[210:213], v[72:75]
	v_mfma_f32_16x16x32_bf16 v[68:71], v[168:171], v[220:223], v[68:71]
	v_mfma_f32_16x16x32_bf16 v[64:67], v[176:179], v[220:223], v[64:67]
	s_setprio 0
	s_barrier
	s_add_i32 s28, s30, s13
	v_lshl_add_u64 v[150:151], s[80:81], 0, v[140:141]
	s_mov_b32 m0, s28
	ds_read_b128 v[180:183], v154 offset:16384
	ds_read_b128 v[184:187], v154 offset:17408
	ds_read_b128 v[188:191], v154 offset:18432
	ds_read_b128 v[192:195], v154 offset:19456
	ds_read_b128 v[206:209], v154 offset:20480
	ds_read_b128 v[210:213], v154 offset:21504
	ds_read_b128 v[216:219], v154 offset:22528
	ds_read_b128 v[220:223], v154 offset:23552
	global_load_lds_dwordx4 v[150:151], off
	s_add_i32 m0, s28, 0x2000
	s_add_u32 s28, s80, 0x40000
	v_lshl_add_u64 v[224:225], s[80:81], 0, v[144:145]
	s_addc_u32 s29, s81, 0
	s_add_i32 s30, s31, s13
	global_load_lds_dwordx4 v[224:225], off
	v_lshl_add_u64 v[226:227], s[28:29], 0, v[140:141]
	s_mov_b32 m0, s30
	v_lshl_add_u64 v[228:229], s[82:83], 0, v[142:143]
	global_load_lds_dwordx4 v[226:227], off
	v_lshl_add_u64 v[226:227], s[28:29], 0, v[144:145]
	s_add_i32 m0, s30, 0x2000
	s_nop 0
	global_load_lds_dwordx4 v[226:227], off
	v_lshl_add_u64 v[226:227], s[82:83], 0, v[138:139]
	s_mov_b32 m0, s26
	s_nop 0
	global_load_lds_dwordx4 v[226:227], off
	s_mov_b32 m0, s27
	s_nop 0
	global_load_lds_dwordx4 v[228:229], off
	s_waitcnt vmcnt(8)
	s_waitcnt lgkmcnt(0)
	s_barrier
	s_setprio 1
	s_waitcnt lgkmcnt(0)
	v_mfma_f32_16x16x32_bf16 v[60:63], v[130:133], v[180:183], 0
	v_mfma_f32_16x16x32_bf16 v[56:59], v[156:159], v[180:183], 0
	v_mfma_f32_16x16x32_bf16 v[52:55], v[130:133], v[188:191], 0
	v_mfma_f32_16x16x32_bf16 v[48:51], v[156:159], v[188:191], 0
	v_mfma_f32_16x16x32_bf16 v[36:39], v[130:133], v[206:209], 0
	v_mfma_f32_16x16x32_bf16 v[32:35], v[156:159], v[206:209], 0
	v_mfma_f32_16x16x32_bf16 v[20:23], v[130:133], v[216:219], 0
	v_mfma_f32_16x16x32_bf16 v[16:19], v[156:159], v[216:219], 0
	v_mfma_f32_16x16x32_bf16 v[60:63], v[134:137], v[184:187], v[60:63]
	v_mfma_f32_16x16x32_bf16 v[56:59], v[160:163], v[184:187], v[56:59]
	v_mfma_f32_16x16x32_bf16 v[52:55], v[134:137], v[192:195], v[52:55]
	v_mfma_f32_16x16x32_bf16 v[48:51], v[160:163], v[192:195], v[48:51]
	v_mfma_f32_16x16x32_bf16 v[36:39], v[134:137], v[210:213], v[36:39]
	v_mfma_f32_16x16x32_bf16 v[32:35], v[160:163], v[210:213], v[32:35]
	v_mfma_f32_16x16x32_bf16 v[20:23], v[134:137], v[220:223], v[20:23]
	v_mfma_f32_16x16x32_bf16 v[16:19], v[160:163], v[220:223], v[16:19]
	s_setprio 0
	s_setprio 1
	v_mfma_f32_16x16x32_bf16 v[44:47], v[164:167], v[180:183], 0
	v_mfma_f32_16x16x32_bf16 v[40:43], v[172:175], v[180:183], 0
	v_mfma_f32_16x16x32_bf16 v[28:31], v[164:167], v[188:191], 0
	v_mfma_f32_16x16x32_bf16 v[24:27], v[172:175], v[188:191], 0
	v_mfma_f32_16x16x32_bf16 v[12:15], v[164:167], v[206:209], 0
	v_mfma_f32_16x16x32_bf16 v[8:11], v[172:175], v[206:209], 0
	v_mfma_f32_16x16x32_bf16 v[4:7], v[164:167], v[216:219], 0
	v_mfma_f32_16x16x32_bf16 v[0:3], v[172:175], v[216:219], 0
	v_mfma_f32_16x16x32_bf16 v[44:47], v[168:171], v[184:187], v[44:47]
	v_mfma_f32_16x16x32_bf16 v[40:43], v[176:179], v[184:187], v[40:43]
	v_mfma_f32_16x16x32_bf16 v[28:31], v[168:171], v[192:195], v[28:31]
	v_mfma_f32_16x16x32_bf16 v[24:27], v[176:179], v[192:195], v[24:27]
	v_mfma_f32_16x16x32_bf16 v[12:15], v[168:171], v[210:213], v[12:15]
	v_mfma_f32_16x16x32_bf16 v[8:11], v[176:179], v[210:213], v[8:11]
	v_mfma_f32_16x16x32_bf16 v[4:7], v[168:171], v[220:223], v[4:7]
	v_mfma_f32_16x16x32_bf16 v[0:3], v[176:179], v[220:223], v[0:3]
	s_setprio 0
	s_barrier
	s_add_i32 s30, 0, 0x18000
	v_add_u32_e32 v112, s30, v153
	s_add_i32 s31, 0, 0x1c000
	ds_read_b128 v[130:133], v112
	ds_read_b128 v[134:137], v112 offset:1024
	ds_read_b128 v[156:159], v112 offset:2048
	ds_read_b128 v[160:163], v112 offset:3072
	v_add_u32_e32 v112, s31, v153
	ds_read_b128 v[164:167], v112
	ds_read_b128 v[168:171], v112 offset:1024
	ds_read_b128 v[172:175], v112 offset:2048
	ds_read_b128 v[176:179], v112 offset:3072
	s_add_u32 s28, s82, 0x40000
	s_addc_u32 s29, s83, 0
	s_mov_b32 m0, s34
	v_lshl_add_u64 v[230:231], s[28:29], 0, v[138:139]
	ds_read_b128 v[180:183], v154 offset:32768
	ds_read_b128 v[184:187], v154 offset:33792
	ds_read_b128 v[188:191], v154 offset:34816
	ds_read_b128 v[192:195], v154 offset:35840
	ds_read_b128 v[206:209], v154 offset:36864
	ds_read_b128 v[210:213], v154 offset:37888
	ds_read_b128 v[216:219], v154 offset:38912
	ds_read_b128 v[220:223], v154 offset:39936
	global_load_lds_dwordx4 v[230:231], off
	v_lshl_add_u64 v[230:231], s[28:29], 0, v[142:143]
	s_mov_b32 m0, s14
	s_nop 0
	global_load_lds_dwordx4 v[230:231], off
	s_waitcnt vmcnt(8)
	s_waitcnt lgkmcnt(0)
	s_barrier
	s_setprio 1
	s_waitcnt lgkmcnt(0)
	v_mfma_f32_16x16x32_bf16 v[126:129], v[130:133], v[180:183], v[126:129]
	v_mfma_f32_16x16x32_bf16 v[122:125], v[156:159], v[180:183], v[122:125]
	v_mfma_f32_16x16x32_bf16 v[118:121], v[130:133], v[188:191], v[118:121]
	v_mfma_f32_16x16x32_bf16 v[114:117], v[156:159], v[188:191], v[114:117]
	v_mfma_f32_16x16x32_bf16 v[100:103], v[130:133], v[206:209], v[100:103]
	v_mfma_f32_16x16x32_bf16 v[96:99], v[156:159], v[206:209], v[96:99]
	v_mfma_f32_16x16x32_bf16 v[84:87], v[130:133], v[216:219], v[84:87]
	v_mfma_f32_16x16x32_bf16 v[80:83], v[156:159], v[216:219], v[80:83]
	v_mfma_f32_16x16x32_bf16 v[126:129], v[134:137], v[184:187], v[126:129]
	v_mfma_f32_16x16x32_bf16 v[122:125], v[160:163], v[184:187], v[122:125]
	v_mfma_f32_16x16x32_bf16 v[118:121], v[134:137], v[192:195], v[118:121]
	v_mfma_f32_16x16x32_bf16 v[114:117], v[160:163], v[192:195], v[114:117]
	v_mfma_f32_16x16x32_bf16 v[100:103], v[134:137], v[210:213], v[100:103]
	v_mfma_f32_16x16x32_bf16 v[96:99], v[160:163], v[210:213], v[96:99]
	v_mfma_f32_16x16x32_bf16 v[84:87], v[134:137], v[220:223], v[84:87]
	v_mfma_f32_16x16x32_bf16 v[80:83], v[160:163], v[220:223], v[80:83]
	s_setprio 0
	s_setprio 1
	v_mfma_f32_16x16x32_bf16 v[108:111], v[164:167], v[180:183], v[108:111]
	v_mfma_f32_16x16x32_bf16 v[104:107], v[172:175], v[180:183], v[104:107]
	v_mfma_f32_16x16x32_bf16 v[92:95], v[164:167], v[188:191], v[92:95]
	v_mfma_f32_16x16x32_bf16 v[88:91], v[172:175], v[188:191], v[88:91]
	v_mfma_f32_16x16x32_bf16 v[76:79], v[164:167], v[206:209], v[76:79]
	v_mfma_f32_16x16x32_bf16 v[72:75], v[172:175], v[206:209], v[72:75]
	v_mfma_f32_16x16x32_bf16 v[68:71], v[164:167], v[216:219], v[68:71]
	v_mfma_f32_16x16x32_bf16 v[64:67], v[172:175], v[216:219], v[64:67]
	v_mfma_f32_16x16x32_bf16 v[108:111], v[168:171], v[184:187], v[108:111]
	v_mfma_f32_16x16x32_bf16 v[104:107], v[176:179], v[184:187], v[104:107]
	v_mfma_f32_16x16x32_bf16 v[92:95], v[168:171], v[192:195], v[92:95]
	v_mfma_f32_16x16x32_bf16 v[88:91], v[176:179], v[192:195], v[88:91]
	v_mfma_f32_16x16x32_bf16 v[76:79], v[168:171], v[210:213], v[76:79]
	v_mfma_f32_16x16x32_bf16 v[72:75], v[176:179], v[210:213], v[72:75]
	v_mfma_f32_16x16x32_bf16 v[68:71], v[168:171], v[220:223], v[68:71]
	v_mfma_f32_16x16x32_bf16 v[64:67], v[176:179], v[220:223], v[64:67]
	s_setprio 0
	s_barrier
	s_add_i32 s28, s30, s13
	v_lshl_add_u64 v[150:151], v[150:151], 0, s[56:57]
	s_mov_b32 m0, s28
	ds_read_b128 v[180:183], v154 offset:49152
	ds_read_b128 v[184:187], v154 offset:50176
	ds_read_b128 v[188:191], v154 offset:51200
	ds_read_b128 v[192:195], v154 offset:52224
	ds_read_b128 v[206:209], v154 offset:53248
	ds_read_b128 v[210:213], v154 offset:54272
	ds_read_b128 v[216:219], v154 offset:55296
	ds_read_b128 v[220:223], v154 offset:56320
	global_load_lds_dwordx4 v[150:151], off
	s_add_i32 m0, s28, 0x2000
	s_add_u32 s28, s80, 0x40080
	v_lshl_add_u64 v[150:151], v[224:225], 0, s[56:57]
	s_addc_u32 s29, s81, 0
	s_add_i32 s30, s31, s13
	global_load_lds_dwordx4 v[150:151], off
	v_lshl_add_u64 v[150:151], s[28:29], 0, v[140:141]
	s_mov_b32 m0, s30
	s_nop 0
	global_load_lds_dwordx4 v[150:151], off
	v_lshl_add_u64 v[150:151], s[28:29], 0, v[144:145]
	s_add_i32 m0, s30, 0x2000
	s_nop 0
	global_load_lds_dwordx4 v[150:151], off
	v_lshl_add_u64 v[150:151], v[226:227], 0, s[56:57]
	s_mov_b32 m0, s33
	s_nop 0
	global_load_lds_dwordx4 v[150:151], off
	v_lshl_add_u64 v[150:151], v[228:229], 0, s[56:57]
	s_mov_b32 m0, s69
	s_nop 0
	global_load_lds_dwordx4 v[150:151], off
	s_waitcnt vmcnt(8)
	s_waitcnt lgkmcnt(0)
	s_barrier
	s_setprio 1
	s_waitcnt lgkmcnt(0)
	v_mfma_f32_16x16x32_bf16 v[60:63], v[130:133], v[180:183], v[60:63]
	v_mfma_f32_16x16x32_bf16 v[56:59], v[156:159], v[180:183], v[56:59]
	v_mfma_f32_16x16x32_bf16 v[52:55], v[130:133], v[188:191], v[52:55]
	v_mfma_f32_16x16x32_bf16 v[48:51], v[156:159], v[188:191], v[48:51]
	v_mfma_f32_16x16x32_bf16 v[36:39], v[130:133], v[206:209], v[36:39]
	v_mfma_f32_16x16x32_bf16 v[32:35], v[156:159], v[206:209], v[32:35]
	v_mfma_f32_16x16x32_bf16 v[20:23], v[130:133], v[216:219], v[20:23]
	v_mfma_f32_16x16x32_bf16 v[16:19], v[156:159], v[216:219], v[16:19]
	v_mfma_f32_16x16x32_bf16 v[60:63], v[134:137], v[184:187], v[60:63]
	v_mfma_f32_16x16x32_bf16 v[56:59], v[160:163], v[184:187], v[56:59]
	v_mfma_f32_16x16x32_bf16 v[52:55], v[134:137], v[192:195], v[52:55]
	v_mfma_f32_16x16x32_bf16 v[48:51], v[160:163], v[192:195], v[48:51]
	v_mfma_f32_16x16x32_bf16 v[36:39], v[134:137], v[210:213], v[36:39]
	v_mfma_f32_16x16x32_bf16 v[32:35], v[160:163], v[210:213], v[32:35]
	v_mfma_f32_16x16x32_bf16 v[20:23], v[134:137], v[220:223], v[20:23]
	v_mfma_f32_16x16x32_bf16 v[16:19], v[160:163], v[220:223], v[16:19]
	s_setprio 0
	s_setprio 1
	v_mfma_f32_16x16x32_bf16 v[44:47], v[164:167], v[180:183], v[44:47]
	v_mfma_f32_16x16x32_bf16 v[40:43], v[172:175], v[180:183], v[40:43]
	v_mfma_f32_16x16x32_bf16 v[28:31], v[164:167], v[188:191], v[28:31]
	v_mfma_f32_16x16x32_bf16 v[24:27], v[172:175], v[188:191], v[24:27]
	v_mfma_f32_16x16x32_bf16 v[12:15], v[164:167], v[206:209], v[12:15]
	v_mfma_f32_16x16x32_bf16 v[8:11], v[172:175], v[206:209], v[8:11]
	v_mfma_f32_16x16x32_bf16 v[4:7], v[164:167], v[216:219], v[4:7]
	v_mfma_f32_16x16x32_bf16 v[0:3], v[172:175], v[216:219], v[0:3]
	v_mfma_f32_16x16x32_bf16 v[44:47], v[168:171], v[184:187], v[44:47]
	v_mfma_f32_16x16x32_bf16 v[40:43], v[176:179], v[184:187], v[40:43]
	v_mfma_f32_16x16x32_bf16 v[28:31], v[168:171], v[192:195], v[28:31]
	v_mfma_f32_16x16x32_bf16 v[24:27], v[176:179], v[192:195], v[24:27]
	v_mfma_f32_16x16x32_bf16 v[12:15], v[168:171], v[210:213], v[12:15]
	v_mfma_f32_16x16x32_bf16 v[8:11], v[176:179], v[210:213], v[8:11]
	v_mfma_f32_16x16x32_bf16 v[4:7], v[168:171], v[220:223], v[4:7]
	v_mfma_f32_16x16x32_bf16 v[0:3], v[176:179], v[220:223], v[0:3]
	s_setprio 0
	s_barrier
	s_add_i32 s71, s71, 2
	s_add_u32 s76, s76, 0x100
	s_addc_u32 s77, s77, 0
	s_add_u32 s51, s51, 0x100
	s_addc_u32 s65, s65, 0
	s_cmp_gt_u32 s71, 13
	.p2align	6

.LBB0_404:
	s_andn2_b64 vcc, exec, s[6:7]
	s_cbranch_vccnz .LBB0_598
	s_mov_b32 s12, s31
	s_mov_b32 s2, s34
	v_mbcnt_lo_u32_b32 v0, -1, 0
	v_mbcnt_hi_u32_b32 v0, -1, v0
	s_cmpk_lt_i32 s12, 0x880
	s_cselect_b64 s[6:7], -1, 0
	s_cmpk_gt_i32 s12, 0x87f
	v_lshl_add_u32 v64, s2, 6, v0
	s_mov_b32 s29, 0x3e6d3388
	s_cbranch_scc1 .LBB0_408
	v_ashrrev_i32_e32 v2, 3, v64
	v_ashrrev_i32_e32 v3, 31, v2
	s_movk_i32 s25, 0xc0
	v_lshlrev_b64 v[16:17], 9, v[2:3]
	v_mul_lo_u32 v2, v2, s25
	v_add_u32_e32 v10, 0, v2
	v_add_u32_e32 v2, 0x200, v64
	v_ashrrev_i32_e32 v2, 3, v2
	v_ashrrev_i32_e32 v3, 31, v2
	v_readlane_b32 s14, v255, 20
	s_lshl_b32 s13, s2, 4
	v_lshlrev_b64 v[18:19], 9, v[2:3]
	v_mul_lo_u32 v2, v2, s25
	v_readlane_b32 s15, v255, 21
	s_lshl_b32 s4, s14, 9
	s_and_b32 s14, s13, 0xffffffe0
	v_ashrrev_i32_e32 v1, 5, v0
	v_add_u32_e32 v11, 0, v2
	v_and_b32_e32 v2, 31, v0
	s_ashr_i32 s15, s14, 31
	v_or_b32_e32 v2, s14, v2
	v_mov_b32_e32 v3, s15
	v_lshlrev_b32_e32 v6, 3, v1
	v_readlane_b32 s14, v253, 62
	v_ashrrev_i32_e32 v7, 31, v6
	v_readlane_b32 s15, v253, 63
	v_and_b32_e32 v12, 16, v0
	v_readlane_b32 s26, v253, 58
	v_lshl_add_u64 v[8:9], v[6:7], 1, s[14:15]
	v_lshrrev_b32_e32 v7, 2, v0
	v_and_or_b32 v6, v7, 3, v6
	s_lshl_b32 s14, s2, 5
	v_lshlrev_b32_e32 v7, 2, v0
	s_and_b32 s15, s14, 32
	v_and_b32_e32 v7, 12, v7
	v_or3_b32 v7, v12, v7, s15
	v_mov_b32_e32 v12, s13
	s_movk_i32 s13, 0xffe0
	v_bfi_b32 v20, s13, v12, v0
	s_lshl_b32 s13, s12, 7
	v_mul_lo_u32 v6, v6, s25
	s_and_b32 s25, s13, 0x180
	v_readlane_b32 s27, v253, 59
	s_add_u32 s13, s26, s25
	s_addc_u32 s14, s27, 0
	s_or_b32 s4, s25, s4
	v_lshl_add_u64 v[2:3], v[2:3], 0, s[4:5]
	v_lshlrev_b64 v[2:3], 8, v[2:3]
	v_lshl_add_u64 v[22:23], v[8:9], 0, v[2:3]
	v_add_u32_e32 v2, s4, v20
	v_readlane_b32 s4, v254, 0
	s_add_u32 s4, s4, s25
	v_readlane_b32 s25, v254, 1
	s_addc_u32 s25, s25, 0
	s_lshl_b32 s15, s15, 1
	v_and_b32_e32 v5, 7, v0
	v_lshlrev_b32_e32 v0, 2, v1
	v_readlane_b32 s36, v253, 40
	s_add_u32 s26, s4, s15
	v_lshlrev_b32_e32 v4, 3, v5
	v_lshlrev_b32_e32 v5, 4, v5
	v_lshl_add_u32 v7, v7, 1, 0
	v_ashrrev_i32_e32 v1, 31, v0
	v_ashrrev_i32_e32 v3, 31, v2
	v_readlane_b32 s37, v253, 41
	s_addc_u32 s27, s25, 0
	v_ashrrev_i32_e32 v21, 31, v20
	v_lshl_add_u64 v[24:25], v[2:3], 2, s[36:37]
	s_mov_b32 s37, s8
	v_readlane_b32 s36, v255, 12
	s_mov_b32 s30, 0x3e027906
	s_mov_b32 s28, 0xbe11a98e
	v_lshl_add_u64 v[26:27], v[0:1], 1, s[26:27]
	v_lshlrev_b32_e32 v112, 1, v4
	v_add_u32_e32 v31, v10, v5
	v_add_u32_e32 v40, v11, v5
	v_add_u32_e32 v41, v7, v6
	s_mov_b32 s4, s12
	v_readlane_b32 s38, v253, 42
	v_readlane_b32 s39, v253, 43
	v_readlane_b32 s40, v253, 44
	v_readlane_b32 s41, v253, 45
	v_readlane_b32 s42, v253, 46
	v_readlane_b32 s43, v253, 47
	.p2align	6

.LBB0_607:
	s_and_b32 s28, s28, 0x10000
	v_add_u32_e32 v65, s28, v61
	ds_read_b128 v[70:73], v65
	ds_read_b128 v[74:77], v65 offset:1024
	ds_read_b128 v[78:81], v65 offset:2048
	ds_read_b128 v[82:85], v65 offset:3072
	ds_read_b128 v[86:89], v65 offset:4096
	ds_read_b128 v[90:93], v65 offset:5120
	ds_read_b128 v[94:97], v65 offset:6144
	ds_read_b128 v[98:101], v65 offset:7168
	ds_read_b128 v[118:121], v65 offset:8192
	ds_read_b128 v[122:125], v65 offset:9216
	ds_read_b128 v[126:129], v65 offset:10240
	ds_read_b128 v[130:133], v65 offset:11264
	ds_read_b128 v[134:137], v65 offset:12288
	ds_read_b128 v[138:141], v65 offset:13312
	ds_read_b128 v[142:145], v65 offset:14336
	s_cmp_lt_u32 s49, 4
	s_movk_i32 s28, 0x11ff
	s_cselect_b32 s28, 0xff, s28
	s_add_i32 s49, s49, 1
	v_cvt_pk_bf16_f32 v20, v0, v1
	v_cvt_pk_bf16_f32 v21, v2, v3
	v_cvt_pk_bf16_f32 v22, v4, v5
	v_cvt_pk_bf16_f32 v23, v6, v7
	v_lshlrev_b32_e32 v32, 16, v28
	v_and_b32_e32 v33, 0xffff0000, v28
	v_lshlrev_b32_e32 v34, 16, v29
	v_and_b32_e32 v35, 0xffff0000, v29
	v_cvt_pk_bf16_f32 v16, v8, v9
	v_cvt_pk_bf16_f32 v17, v10, v11
	v_cvt_pk_bf16_f32 v18, v12, v13
	v_cvt_pk_bf16_f32 v19, v14, v15
	v_lshlrev_b32_e32 v28, 16, v30
	v_and_b32_e32 v29, 0xffff0000, v30
	v_lshlrev_b32_e32 v30, 16, v31
	v_and_b32_e32 v31, 0xffff0000, v31
	v_lshlrev_b32_e32 v36, 16, v24
	v_and_b32_e32 v37, 0xffff0000, v24
	v_lshlrev_b32_e32 v38, 16, v25
	v_and_b32_e32 v39, 0xffff0000, v25
	v_lshlrev_b32_e32 v24, 16, v26
	v_and_b32_e32 v25, 0xffff0000, v26
	v_lshlrev_b32_e32 v26, 16, v27
	v_and_b32_e32 v27, 0xffff0000, v27
	s_waitcnt lgkmcnt(7)
	s_nop 1
	v_mfma_f32_16x16x32_bf16 v[32:35], v[70:73], v[20:23], v[32:35]
	v_mfma_f32_16x16x32_bf16 v[28:31], v[78:81], v[20:23], v[28:31]
	v_mfma_f32_16x16x32_bf16 v[36:39], v[86:89], v[20:23], v[36:39]
	v_mfma_f32_16x16x32_bf16 v[24:27], v[94:97], v[20:23], v[24:27]
	v_mfma_f32_16x16x32_bf16 v[32:35], v[74:77], v[16:19], v[32:35]
	v_mfma_f32_16x16x32_bf16 v[40:43], v[82:85], v[16:19], v[28:31]
	v_mfma_f32_16x16x32_bf16 v[36:39], v[90:93], v[16:19], v[36:39]
	v_mfma_f32_16x16x32_bf16 v[66:69], v[98:101], v[16:19], v[24:27]
	s_waitcnt lgkmcnt(0)
	ds_read_b128 v[146:149], v65 offset:15360
	ds_read_b128 v[102:105], v65 offset:16384
	ds_read_b128 v[106:109], v65 offset:17408
	ds_read_b128 v[150:153], v65 offset:18432
	ds_read_b128 v[154:157], v65 offset:19456
	ds_read_b128 v[158:161], v65 offset:20480
	ds_read_b128 v[162:165], v65 offset:21504
	ds_read_b128 v[206:209], v65 offset:22528
	ds_read_b128 v[210:213], v65 offset:23552
	ds_read_b128 v[226:229], v65 offset:24576
	ds_read_b128 v[230:233], v65 offset:25600
	ds_read_b128 v[234:237], v65 offset:26624
	ds_read_b128 v[238:241], v65 offset:27648
	ds_read_b128 v[242:245], v65 offset:28672
	v_pk_mul_f32 v[2:3], v[2:3], v[58:59] op_sel_hi:[1,0]
	v_pk_mul_f32 v[0:1], v[0:1], v[58:59] op_sel_hi:[1,0]
	v_pk_mul_f32 v[6:7], v[6:7], v[58:59] op_sel_hi:[1,0]
	v_pk_mul_f32 v[4:5], v[4:5], v[58:59] op_sel_hi:[1,0]
	v_pk_mul_f32 v[10:11], v[10:11], v[58:59] op_sel_hi:[1,0]
	v_pk_mul_f32 v[8:9], v[8:9], v[58:59] op_sel_hi:[1,0]
	v_pk_mul_f32 v[14:15], v[14:15], v[58:59] op_sel_hi:[1,0]
	v_pk_mul_f32 v[12:13], v[12:13], v[58:59] op_sel_hi:[1,0]
	v_cvt_pk_bf16_f32 v28, v32, v33
	v_cvt_pk_bf16_f32 v29, v34, v35
	v_cvt_pk_bf16_f32 v30, v40, v41
	v_cvt_pk_bf16_f32 v31, v42, v43
	v_cvt_pk_bf16_f32 v24, v36, v37
	v_cvt_pk_bf16_f32 v25, v38, v39
	v_cvt_pk_bf16_f32 v26, v66, v67
	v_cvt_pk_bf16_f32 v27, v68, v69
	s_waitcnt lgkmcnt(0)
	ds_read_b128 v[70:73], v65 offset:29696
	ds_read_b128 v[74:77], v65 offset:30720
	ds_read_b128 v[78:81], v65 offset:31744
	s_nop 0
	v_mfma_f32_16x16x32_bf16 v[32:35], v[118:121], v[20:23], 0
	v_mfma_f32_16x16x32_bf16 v[40:43], v[126:129], v[20:23], 0
	v_mfma_f32_16x16x32_bf16 v[32:35], v[102:105], v[28:31], v[32:35]
	v_mfma_f32_16x16x32_bf16 v[40:43], v[150:153], v[28:31], v[40:43]
	v_mfma_f32_16x16x32_bf16 v[32:35], v[122:125], v[16:19], v[32:35]
	v_mfma_f32_16x16x32_bf16 v[40:43], v[130:133], v[16:19], v[40:43]
	v_mfma_f32_16x16x32_bf16 v[36:39], v[106:109], v[24:27], v[32:35]
	v_mfma_f32_16x16x32_bf16 v[40:43], v[154:157], v[24:27], v[40:43]
	v_mfma_f32_16x16x32_bf16 v[32:35], v[134:137], v[20:23], 0
	v_mfma_f32_16x16x32_bf16 v[32:35], v[158:161], v[28:31], v[32:35]
	v_mfma_f32_16x16x32_bf16 v[32:35], v[138:141], v[16:19], v[32:35]
	v_mfma_f32_16x16x32_bf16 v[32:35], v[162:165], v[24:27], v[32:35]
	v_mfma_f32_16x16x32_bf16 v[20:23], v[142:145], v[20:23], 0
	v_mfma_f32_16x16x32_bf16 v[20:23], v[206:209], v[28:31], v[20:23]
	v_mfma_f32_16x16x32_bf16 v[16:19], v[146:149], v[16:19], v[20:23]
	v_mfma_f32_16x16x32_bf16 v[16:19], v[210:213], v[24:27], v[16:19]
	s_waitcnt lgkmcnt(0)
	v_mfma_f32_16x16x32_bf16 v[0:3], v[226:229], v[28:31], v[0:3]
	v_mfma_f32_16x16x32_bf16 v[4:7], v[234:237], v[28:31], v[4:7]
	v_mfma_f32_16x16x32_bf16 v[8:11], v[242:245], v[28:31], v[8:11]
	v_mfma_f32_16x16x32_bf16 v[12:15], v[74:77], v[28:31], v[12:15]
	v_mfma_f32_16x16x32_bf16 v[0:3], v[230:233], v[24:27], v[0:3]
	v_mfma_f32_16x16x32_bf16 v[4:7], v[238:241], v[24:27], v[4:7]
	v_mfma_f32_16x16x32_bf16 v[8:11], v[70:73], v[24:27], v[8:11]
	v_mfma_f32_16x16x32_bf16 v[12:15], v[78:81], v[24:27], v[12:15]
	v_cvt_pk_bf16_f32 v16, v16, s0
	v_cvt_pk_bf16_f32 v18, v18, s0
	v_add_u32_e32 v24, s28, v64
	v_add_u32_e32 v22, s48, v60
	v_add_u32_e32 v20, 51, v24
	v_cndmask_b32_e64 v20, v20, v22, s[38:39]
	v_ashrrev_i32_e32 v21, 31, v20
	v_lshl_add_u64 v[20:21], s[6:7], 0, v[20:21]
	v_lshlrev_b64 v[20:21], 9, v[20:21]
	v_cvt_pk_bf16_f32 v23, v36, s0
	v_lshl_add_u64 v[20:21], v[48:49], 0, v[20:21]
	global_store_short v[20:21], v23, off
	v_add_u32_e32 v20, 1, v22
	v_add_u32_e32 v21, 50, v24
	v_cndmask_b32_e64 v20, v21, v20, s[38:39]
	v_ashrrev_i32_e32 v21, 31, v20
	v_lshl_add_u64 v[20:21], s[6:7], 0, v[20:21]
	v_lshlrev_b64 v[20:21], 9, v[20:21]
	v_cvt_pk_bf16_f32 v23, v37, s0
	v_lshl_add_u64 v[20:21], v[48:49], 0, v[20:21]
	global_store_short v[20:21], v23, off
	v_add_u32_e32 v20, 2, v22
	v_add_u32_e32 v21, 49, v24
	v_cndmask_b32_e64 v20, v21, v20, s[38:39]
	v_ashrrev_i32_e32 v21, 31, v20
	v_lshl_add_u64 v[20:21], s[6:7], 0, v[20:21]
	v_lshlrev_b64 v[20:21], 9, v[20:21]
	v_cvt_pk_bf16_f32 v23, v38, s0
	v_lshl_add_u64 v[20:21], v[48:49], 0, v[20:21]
	global_store_short v[20:21], v23, off
	v_add_u32_e32 v20, 3, v22
	v_add_u32_e32 v21, 48, v24
	v_cndmask_b32_e64 v20, v21, v20, s[38:39]
	v_ashrrev_i32_e32 v21, 31, v20
	v_lshl_add_u64 v[20:21], s[6:7], 0, v[20:21]
	v_lshlrev_b64 v[20:21], 9, v[20:21]
	v_cvt_pk_bf16_f32 v23, v39, s0
	v_lshl_add_u64 v[20:21], v[48:49], 0, v[20:21]
	global_store_short v[20:21], v23, off
	v_add_u32_e32 v20, 16, v22
	v_add_u32_e32 v21, 35, v24
	v_cndmask_b32_e64 v20, v21, v20, s[38:39]
	v_ashrrev_i32_e32 v21, 31, v20
	v_lshl_add_u64 v[20:21], s[6:7], 0, v[20:21]
	v_lshlrev_b64 v[20:21], 9, v[20:21]
	v_cvt_pk_bf16_f32 v23, v40, s0
	v_lshl_add_u64 v[20:21], v[48:49], 0, v[20:21]
	global_store_short v[20:21], v23, off
	v_add_u32_e32 v20, 17, v22
	v_add_u32_e32 v21, 34, v24
	v_cndmask_b32_e64 v20, v21, v20, s[38:39]
	v_ashrrev_i32_e32 v21, 31, v20
	v_lshl_add_u64 v[20:21], s[6:7], 0, v[20:21]
	v_lshlrev_b64 v[20:21], 9, v[20:21]
	v_cvt_pk_bf16_f32 v23, v41, s0
	v_lshl_add_u64 v[20:21], v[48:49], 0, v[20:21]
	global_store_short v[20:21], v23, off
	v_add_u32_e32 v20, 18, v22
	v_add_u32_e32 v21, 33, v24
	v_cndmask_b32_e64 v20, v21, v20, s[38:39]
	v_ashrrev_i32_e32 v21, 31, v20
	v_lshl_add_u64 v[20:21], s[6:7], 0, v[20:21]
	v_lshlrev_b64 v[20:21], 9, v[20:21]
	v_cvt_pk_bf16_f32 v23, v42, s0
	v_lshl_add_u64 v[20:21], v[48:49], 0, v[20:21]
	global_store_short v[20:21], v23, off
	v_add_u32_e32 v20, 19, v22
	v_add_u32_e32 v21, 32, v24
	v_cndmask_b32_e64 v20, v21, v20, s[38:39]
	v_ashrrev_i32_e32 v21, 31, v20
	v_lshl_add_u64 v[20:21], s[6:7], 0, v[20:21]
	v_lshlrev_b64 v[20:21], 9, v[20:21]
	v_cvt_pk_bf16_f32 v23, v43, s0
	v_lshl_add_u64 v[20:21], v[48:49], 0, v[20:21]
	global_store_short v[20:21], v23, off
	v_add_u32_e32 v20, 32, v22
	v_add_u32_e32 v21, 19, v24
	v_cndmask_b32_e64 v20, v21, v20, s[38:39]
	v_ashrrev_i32_e32 v21, 31, v20
	v_lshl_add_u64 v[20:21], s[6:7], 0, v[20:21]
	v_lshlrev_b64 v[20:21], 9, v[20:21]
	v_cvt_pk_bf16_f32 v23, v32, s0
	v_lshl_add_u64 v[20:21], v[48:49], 0, v[20:21]
	global_store_short v[20:21], v23, off
	v_add_u32_e32 v20, 33, v22
	v_add_u32_e32 v21, 18, v24
	v_cndmask_b32_e64 v20, v21, v20, s[38:39]
	v_ashrrev_i32_e32 v21, 31, v20
	v_lshl_add_u64 v[20:21], s[6:7], 0, v[20:21]
	v_lshlrev_b64 v[20:21], 9, v[20:21]
	v_cvt_pk_bf16_f32 v23, v33, s0
	v_lshl_add_u64 v[20:21], v[48:49], 0, v[20:21]
	global_store_short v[20:21], v23, off
	v_add_u32_e32 v20, 34, v22
	v_add_u32_e32 v21, 17, v24
	v_cndmask_b32_e64 v20, v21, v20, s[38:39]
	v_ashrrev_i32_e32 v21, 31, v20
	v_lshl_add_u64 v[20:21], s[6:7], 0, v[20:21]
	v_lshlrev_b64 v[20:21], 9, v[20:21]
	v_cvt_pk_bf16_f32 v23, v34, s0
	v_lshl_add_u64 v[20:21], v[48:49], 0, v[20:21]
	global_store_short v[20:21], v23, off
	v_add_u32_e32 v20, 35, v22
	v_add_u32_e32 v21, 16, v24
	v_cndmask_b32_e64 v20, v21, v20, s[38:39]
	v_ashrrev_i32_e32 v21, 31, v20
	v_lshl_add_u64 v[20:21], s[6:7], 0, v[20:21]
	v_lshlrev_b64 v[20:21], 9, v[20:21]
	v_cvt_pk_bf16_f32 v23, v35, s0
	v_lshl_add_u64 v[20:21], v[48:49], 0, v[20:21]
	global_store_short v[20:21], v23, off
	v_add_u32_e32 v20, 48, v22
	v_add_u32_e32 v21, 3, v24
	v_cndmask_b32_e64 v20, v21, v20, s[38:39]
	v_ashrrev_i32_e32 v21, 31, v20
	v_lshl_add_u64 v[20:21], s[6:7], 0, v[20:21]
	v_lshlrev_b64 v[20:21], 9, v[20:21]
	v_lshl_add_u64 v[20:21], v[48:49], 0, v[20:21]
	global_store_short v[20:21], v16, off
	v_cvt_pk_bf16_f32 v20, v17, s0
	v_add_u32_e32 v16, 49, v22
	v_add_u32_e32 v17, 2, v24
	v_cndmask_b32_e64 v16, v17, v16, s[38:39]
	v_ashrrev_i32_e32 v17, 31, v16
	v_lshl_add_u64 v[16:17], s[6:7], 0, v[16:17]
	v_lshlrev_b64 v[16:17], 9, v[16:17]
	v_lshl_add_u64 v[16:17], v[48:49], 0, v[16:17]
	global_store_short v[16:17], v20, off
	v_add_u32_e32 v16, 50, v22
	v_add_u32_e32 v17, 1, v24
	v_cndmask_b32_e64 v16, v17, v16, s[38:39]
	v_ashrrev_i32_e32 v17, 31, v16
	v_lshl_add_u64 v[16:17], s[6:7], 0, v[16:17]
	v_lshlrev_b64 v[16:17], 9, v[16:17]
	v_lshl_add_u64 v[16:17], v[48:49], 0, v[16:17]
	global_store_short v[16:17], v18, off
	v_add_u32_e32 v16, 51, v22
	v_cndmask_b32_e64 v16, v24, v16, s[38:39]
	v_ashrrev_i32_e32 v17, 31, v16
	v_lshl_add_u64 v[16:17], s[6:7], 0, v[16:17]
	v_lshlrev_b64 v[16:17], 9, v[16:17]
	s_add_i32 s48, s48, 64
	v_cvt_pk_bf16_f32 v18, v19, s0
	v_lshl_add_u64 v[16:17], v[48:49], 0, v[16:17]
	v_subrev_u32_e32 v64, 64, v64
	s_cmpk_eq_i32 s48, 0x1100
	s_mov_b32 s28, s43
	global_store_short v[16:17], v18, off
	s_cbranch_scc1 .LBB0_612
	.p2align	6

.LBB0_631:
	v_pk_mul_f32 v[0:1], v[106:107], s[58:59] op_sel_hi:[1,0]
	s_and_b64 s[28:29], s[72:73], exec
	v_cvt_pk_bf16_f32 v118, v0, v1
	v_pk_mul_f32 v[0:1], v[102:103], s[58:59] op_sel_hi:[1,0]
	s_cselect_b32 s4, -2, 0xffffffbe
	v_cvt_pk_bf16_f32 v119, v0, v1
	v_pk_mul_f32 v[0:1], v[36:37], s[58:59] op_sel_hi:[1,0]
	s_add_u32 s28, s27, s12
	v_cvt_pk_bf16_f32 v120, v0, v1
	v_pk_mul_f32 v[0:1], v[32:33], s[58:59] op_sel_hi:[1,0]
	s_addc_u32 s29, 0, 0
	v_cvt_pk_bf16_f32 v121, v0, v1
	v_pk_mul_f32 v[0:1], v[28:29], s[58:59] op_sel_hi:[1,0]
	s_lshr_b64 s[28:29], s[28:29], 1
	v_cvt_pk_bf16_f32 v122, v0, v1
	v_pk_mul_f32 v[0:1], v[30:31], s[58:59] op_sel_hi:[1,0]
	s_mul_i32 s13, s28, 0x220000
	v_cvt_pk_bf16_f32 v123, v0, v1
	v_pk_mul_f32 v[0:1], v[24:25], s[58:59] op_sel_hi:[1,0]
	s_mul_hi_u32 s29, s28, 0x220000
	v_cvt_pk_bf16_f32 v124, v0, v1
	v_pk_mul_f32 v[0:1], v[26:27], s[58:59] op_sel_hi:[1,0]
	s_or_b32 s28, s13, s70
	v_cvt_pk_bf16_f32 v125, v0, v1
	v_pk_mul_f32 v[0:1], v[90:91], s[58:59] op_sel_hi:[1,0]
	v_mov_b32_e32 v32, 0
	v_cvt_pk_bf16_f32 v126, v0, v1
	v_pk_mul_f32 v[0:1], v[38:39], s[58:59] op_sel_hi:[1,0]
	s_mov_b32 s12, 1
	v_cvt_pk_bf16_f32 v127, v0, v1
	v_pk_mul_f32 v[0:1], v[34:35], s[58:59] op_sel_hi:[1,0]
	v_lshl_add_u64 v[194:195], v[188:189], 0, s[28:29]
	v_cvt_pk_bf16_f32 v128, v0, v1
	v_pk_mul_f32 v[0:1], v[18:19], s[58:59] op_sel_hi:[1,0]
	v_mov_b32_e32 v33, v32
	v_cvt_pk_bf16_f32 v129, v0, v1
	v_pk_mul_f32 v[0:1], v[16:17], s[58:59] op_sel_hi:[1,0]
	v_mov_b32_e32 v34, v32
	v_cvt_pk_bf16_f32 v130, v0, v1
	v_pk_mul_f32 v[0:1], v[14:15], s[58:59] op_sel_hi:[1,0]
	v_mov_b32_e32 v35, v32
	v_cvt_pk_bf16_f32 v131, v0, v1
	v_pk_mul_f32 v[0:1], v[12:13], s[58:59] op_sel_hi:[1,0]
	v_mov_b32_e32 v36, v32
	v_cvt_pk_bf16_f32 v132, v0, v1
	v_pk_mul_f32 v[0:1], v[20:21], s[58:59] op_sel_hi:[1,0]
	v_mov_b32_e32 v37, v32
	v_cvt_pk_bf16_f32 v133, v0, v1
	v_pk_mul_f32 v[0:1], v[78:79], s[58:59] op_sel_hi:[1,0]
	v_mov_b32_e32 v38, v32
	v_cvt_pk_bf16_f32 v134, v0, v1
	v_pk_mul_f32 v[0:1], v[74:75], s[58:59] op_sel_hi:[1,0]
	v_mov_b32_e32 v39, v32
	v_cvt_pk_bf16_f32 v135, v0, v1
	v_pk_mul_f32 v[0:1], v[70:71], s[58:59] op_sel_hi:[1,0]
	v_mov_b32_e32 v40, v32
	v_cvt_pk_bf16_f32 v136, v0, v1
	v_pk_mul_f32 v[0:1], v[66:67], s[58:59] op_sel_hi:[1,0]
	v_mov_b32_e32 v41, v32
	v_cvt_pk_bf16_f32 v137, v0, v1
	v_pk_mul_f32 v[0:1], v[56:57], s[58:59] op_sel_hi:[1,0]
	v_mov_b32_e32 v42, v32
	v_cvt_pk_bf16_f32 v138, v0, v1
	v_pk_mul_f32 v[0:1], v[60:61], s[58:59] op_sel_hi:[1,0]
	v_mov_b32_e32 v43, v32
	v_cvt_pk_bf16_f32 v139, v0, v1
	v_pk_mul_f32 v[0:1], v[52:53], s[58:59] op_sel_hi:[1,0]
	v_mov_b32_e32 v48, v32
	v_cvt_pk_bf16_f32 v140, v0, v1
	v_pk_mul_f32 v[0:1], v[58:59], s[58:59] op_sel_hi:[1,0]
	v_mov_b32_e32 v49, v32
	v_cvt_pk_bf16_f32 v141, v0, v1
	v_pk_mul_f32 v[0:1], v[76:77], s[58:59] op_sel_hi:[1,0]
	v_mov_b32_e32 v50, v32
	v_cvt_pk_bf16_f32 v142, v0, v1
	v_pk_mul_f32 v[0:1], v[72:73], s[58:59] op_sel_hi:[1,0]
	v_mov_b32_e32 v51, v32
	v_cvt_pk_bf16_f32 v143, v0, v1
	v_pk_mul_f32 v[0:1], v[68:69], s[58:59] op_sel_hi:[1,0]
	v_mov_b32_e32 v52, v32
	v_cvt_pk_bf16_f32 v144, v0, v1
	v_pk_mul_f32 v[0:1], v[62:63], s[58:59] op_sel_hi:[1,0]
	v_mov_b32_e32 v53, v32
	v_cvt_pk_bf16_f32 v145, v0, v1
	v_pk_mul_f32 v[0:1], v[46:47], s[58:59] op_sel_hi:[1,0]
	v_mov_b32_e32 v46, v32
	v_cvt_pk_bf16_f32 v146, v0, v1
	v_pk_mul_f32 v[0:1], v[54:55], s[58:59] op_sel_hi:[1,0]
	v_mov_b32_e32 v47, v32
	v_cvt_pk_bf16_f32 v147, v0, v1
	v_pk_mul_f32 v[0:1], v[44:45], s[58:59] op_sel_hi:[1,0]
	v_mov_b32_e32 v44, v32
	v_cvt_pk_bf16_f32 v148, v0, v1
	v_pk_mul_f32 v[0:1], v[64:65], s[58:59] op_sel_hi:[1,0]
	v_mov_b32_e32 v45, v32
	v_cvt_pk_bf16_f32 v149, v0, v1
	v_mov_b32_e32 v54, v32
	v_mov_b32_e32 v55, v32
	v_mov_b32_e32 v56, v32
	v_mov_b32_e32 v57, v32
	v_mov_b32_e32 v58, v32
	v_mov_b32_e32 v59, v32
	v_mov_b32_e32 v60, v32
	v_mov_b32_e32 v61, v32
	v_mov_b32_e32 v62, v32
	v_mov_b32_e32 v63, v32
	v_mov_b32_e32 v154, v32
	v_mov_b32_e32 v155, v32
	v_mov_b32_e32 v156, v32
	v_mov_b32_e32 v157, v32
	v_mov_b32_e32 v150, v32
	v_mov_b32_e32 v151, v32
	v_mov_b32_e32 v152, v32
	v_mov_b32_e32 v153, v32
	v_mov_b32_e32 v16, v32
	v_mov_b32_e32 v17, v32
	v_mov_b32_e32 v18, v32
	v_mov_b32_e32 v19, v32
	v_mov_b32_e32 v20, v32
	v_mov_b32_e32 v21, v32
	v_mov_b32_e32 v22, v32
	v_mov_b32_e32 v23, v32
	v_mov_b32_e32 v24, v32
	v_mov_b32_e32 v25, v32
	v_mov_b32_e32 v26, v32
	v_mov_b32_e32 v27, v32
	v_mov_b32_e32 v28, v32
	v_mov_b32_e32 v29, v32
	v_mov_b32_e32 v30, v32
	v_mov_b32_e32 v31, v32
	v_mov_b32_e32 v0, v32
	v_mov_b32_e32 v1, v32
	v_mov_b32_e32 v2, v32
	v_mov_b32_e32 v3, v32
	v_mov_b32_e32 v4, v32
	v_mov_b32_e32 v5, v32
	v_mov_b32_e32 v6, v32
	v_mov_b32_e32 v7, v32
	v_mov_b32_e32 v8, v32
	v_mov_b32_e32 v9, v32
	v_mov_b32_e32 v10, v32
	v_mov_b32_e32 v11, v32
	v_mov_b32_e32 v12, v32
	v_mov_b32_e32 v13, v32
	v_mov_b32_e32 v14, v32
	v_mov_b32_e32 v15, v32
	s_mov_b32 s69, s68
	s_mov_b32 s70, s68
	s_mov_b32 s71, s68
	s_mov_b32 s72, s68
	s_mov_b32 s73, s68
	s_mov_b32 s74, s68
	s_mov_b32 s75, s68
	s_mov_b32 s76, s68
	s_mov_b32 s77, s68
	s_mov_b32 s78, s68
	s_mov_b32 s79, s68
	s_mov_b32 s80, s68
	s_mov_b32 s81, s68
	s_mov_b32 s82, s68
	s_mov_b32 s83, s68
	.p2align	6

.LBB0_641:
	v_pk_mul_f32 v[0:1], v[24:25], s[60:61] op_sel_hi:[1,0]
	s_lshl_b32 s14, s12, 6
	v_cvt_pk_bf16_f32 v118, v0, v1
	v_pk_mul_f32 v[0:1], v[28:29], s[60:61] op_sel_hi:[1,0]
	s_and_b64 s[12:13], s[70:71], exec
	v_cvt_pk_bf16_f32 v119, v0, v1
	v_pk_mul_f32 v[0:1], v[20:21], s[60:61] op_sel_hi:[1,0]
	s_cselect_b32 s4, -2, 0xffffffbe
	v_cvt_pk_bf16_f32 v120, v0, v1
	v_pk_mul_f32 v[0:1], v[22:23], s[60:61] op_sel_hi:[1,0]
	s_lshl_b32 s14, s14, 1
	v_cvt_pk_bf16_f32 v121, v0, v1
	v_pk_mul_f32 v[0:1], v[30:31], s[60:61] op_sel_hi:[1,0]
	s_mul_i32 s12, s2, 0x220000
	v_cvt_pk_bf16_f32 v122, v0, v1
	v_pk_mul_f32 v[0:1], v[34:35], s[60:61] op_sel_hi:[1,0]
	s_and_b32 s14, s14, 0x180
	v_cvt_pk_bf16_f32 v123, v0, v1
	v_pk_mul_f32 v[0:1], v[26:27], s[60:61] op_sel_hi:[1,0]
	s_mul_hi_i32 s13, s2, 0x220000
	v_cvt_pk_bf16_f32 v124, v0, v1
	v_pk_mul_f32 v[0:1], v[32:33], s[60:61] op_sel_hi:[1,0]
	s_or_b32 s12, s12, s14
	v_cvt_pk_bf16_f32 v125, v0, v1
	v_pk_mul_f32 v[0:1], v[38:39], s[60:61] op_sel_hi:[1,0]
	s_mov_b32 s2, 1
	v_cvt_pk_bf16_f32 v126, v0, v1
	v_pk_mul_f32 v[0:1], v[44:45], s[60:61] op_sel_hi:[1,0]
	v_lshl_add_u64 v[152:153], v[190:191], 0, s[12:13]
	v_cvt_pk_bf16_f32 v127, v0, v1
	v_pk_mul_f32 v[0:1], v[36:37], s[60:61] op_sel_hi:[1,0]
	s_nop 0
	v_cvt_pk_bf16_f32 v128, v0, v1
	v_pk_mul_f32 v[0:1], v[40:41], s[60:61] op_sel_hi:[1,0]
	s_nop 0
	v_cvt_pk_bf16_f32 v129, v0, v1
	v_pk_mul_f32 v[0:1], v[46:47], s[60:61] op_sel_hi:[1,0]
	s_nop 0
	v_cvt_pk_bf16_f32 v130, v0, v1
	v_pk_mul_f32 v[0:1], v[50:51], s[60:61] op_sel_hi:[1,0]
	s_nop 0
	v_cvt_pk_bf16_f32 v131, v0, v1
	v_pk_mul_f32 v[0:1], v[42:43], s[60:61] op_sel_hi:[1,0]
	s_nop 0
	v_cvt_pk_bf16_f32 v132, v0, v1
	v_pk_mul_f32 v[0:1], v[48:49], s[60:61] op_sel_hi:[1,0]
	s_nop 0
	v_cvt_pk_bf16_f32 v133, v0, v1
	v_mov_b32_e32 v0, 0
	v_mov_b32_e32 v1, v0
	v_mov_b32_e32 v2, v0
	v_mov_b32_e32 v3, v0
	v_mov_b32_e32 v4, v0
	v_mov_b32_e32 v5, v0
	v_mov_b32_e32 v6, v0
	v_mov_b32_e32 v7, v0
	v_mov_b32_e32 v8, v0
	v_mov_b32_e32 v9, v0
	v_mov_b32_e32 v10, v0
	v_mov_b32_e32 v11, v0
	v_mov_b32_e32 v12, v0
	v_mov_b32_e32 v13, v0
	v_mov_b32_e32 v14, v0
	v_mov_b32_e32 v15, v0
	v_mov_b32_e32 v32, v0
	v_mov_b32_e32 v33, v0
	v_mov_b32_e32 v34, v0
	v_mov_b32_e32 v35, v0
	v_mov_b32_e32 v36, v0
	v_mov_b32_e32 v37, v0
	v_mov_b32_e32 v38, v0
	v_mov_b32_e32 v39, v0
	v_mov_b32_e32 v40, v0
	v_mov_b32_e32 v41, v0
	v_mov_b32_e32 v42, v0
	v_mov_b32_e32 v43, v0
	v_mov_b32_e32 v44, v0
	v_mov_b32_e32 v45, v0
	v_mov_b32_e32 v46, v0
	v_mov_b32_e32 v47, v0
	v_mov_b32_e32 v138, v0
	v_mov_b32_e32 v139, v0
	v_mov_b32_e32 v140, v0
	v_mov_b32_e32 v141, v0
	v_mov_b32_e32 v134, v0
	v_mov_b32_e32 v135, v0
	v_mov_b32_e32 v136, v0
	v_mov_b32_e32 v137, v0
	v_mov_b32_e32 v48, v0
	v_mov_b32_e32 v49, v0
	v_mov_b32_e32 v50, v0
	v_mov_b32_e32 v51, v0
	v_mov_b32_e32 v52, v0
	v_mov_b32_e32 v53, v0
	v_mov_b32_e32 v54, v0
	v_mov_b32_e32 v55, v0
	v_mov_b32_e32 v56, v0
	v_mov_b32_e32 v57, v0
	v_mov_b32_e32 v58, v0
	v_mov_b32_e32 v59, v0
	v_mov_b32_e32 v60, v0
	v_mov_b32_e32 v61, v0
	v_mov_b32_e32 v62, v0
	v_mov_b32_e32 v63, v0
	v_mov_b32_e32 v16, v0
	v_mov_b32_e32 v17, v0
	v_mov_b32_e32 v18, v0
	v_mov_b32_e32 v19, v0
	v_mov_b32_e32 v20, v0
	v_mov_b32_e32 v21, v0
	v_mov_b32_e32 v22, v0
	v_mov_b32_e32 v23, v0
	v_mov_b32_e32 v24, v0
	v_mov_b32_e32 v25, v0
	v_mov_b32_e32 v26, v0
	v_mov_b32_e32 v27, v0
	v_mov_b32_e32 v28, v0
	v_mov_b32_e32 v29, v0
	v_mov_b32_e32 v30, v0
	v_mov_b32_e32 v31, v0
	s_mov_b32 s69, s68
	s_mov_b32 s70, s68
	s_mov_b32 s71, s68
	s_mov_b32 s72, s68
	s_mov_b32 s73, s68
	s_mov_b32 s74, s68
	s_mov_b32 s75, s68
	s_mov_b32 s76, s68
	s_mov_b32 s77, s68
	s_mov_b32 s78, s68
	s_mov_b32 s79, s68
	s_mov_b32 s80, s68
	s_mov_b32 s81, s68
	s_mov_b32 s82, s68
	s_mov_b32 s83, s68
	.p2align	6

.Lpeel_gate:
	s_add_u32 s28, s82, 0xfffe0080
	s_addc_u32 s29, s83, -1
	s_add_i32 s85, 0, 0x10000
	s_cmp_eq_u32 s84, 4
	s_cselect_b32 vcc_hi, s37, s29
	s_cselect_b32 vcc_lo, s50, s28
	s_cselect_b32 s97, s51, s75
	s_cselect_b32 s96, s71, s73
	s_add_i32 s28, 0, 0x14000
	v_add_u32_e32 v0, s85, v183
	v_add_u32_e32 v12, s28, v183
	ds_read_b128 v[16:19], v0
	ds_read_b128 v[20:23], v0 offset:1024
	ds_read_b128 v[24:27], v0 offset:2048
	ds_read_b128 v[28:31], v0 offset:3072
	ds_read_b128 v[0:3], v12
	ds_read_b128 v[4:7], v12 offset:1024
	ds_read_b128 v[8:11], v12 offset:2048
	ds_read_b128 v[12:15], v12 offset:3072
	v_lshl_add_u64 v[194:195], s[82:83], 0, v[170:171]
	s_add_i32 m0, s6, 0xc000
	ds_read_b128 v[174:177], v184
	ds_read_b128 v[178:181], v184 offset:1024
	ds_read_b128 v[186:189], v184 offset:2048
	ds_read_b128 v[190:193], v184 offset:3072
	ds_read_b128 v[216:219], v184 offset:4096
	ds_read_b128 v[220:223], v184 offset:5120
	ds_read_b128 v[224:227], v184 offset:6144
	ds_read_b128 v[228:231], v184 offset:7168
	global_load_lds_dwordx4 v[194:195], off
	v_lshl_add_u64 v[194:195], s[82:83], 0, v[172:173]
	s_add_i32 m0, s6, 0xe000
	s_nop 0
	global_load_lds_dwordx4 v[194:195], off
	s_waitcnt vmcnt(8)
	s_waitcnt lgkmcnt(0)
	s_barrier
	s_setprio 1
	s_waitcnt lgkmcnt(0)
	v_mfma_scale_f32_16x16x128_f8f6f4 v[158:161], v[16:23], v[174:181], 0, v200, v201 op_sel_hi:[0,0,0]
	v_mfma_scale_f32_16x16x128_f8f6f4 v[154:157], v[24:31], v[174:181], 0, v200, v201 op_sel_hi:[0,0,0]
	v_mfma_scale_f32_16x16x128_f8f6f4 v[150:153], v[16:23], v[186:193], 0, v200, v201 op_sel_hi:[0,0,0]
	v_mfma_scale_f32_16x16x128_f8f6f4 v[146:149], v[24:31], v[186:193], 0, v200, v201 op_sel_hi:[0,0,0]
	v_mfma_scale_f32_16x16x128_f8f6f4 v[134:137], v[16:23], v[216:223], 0, v200, v201 op_sel_hi:[0,0,0]
	v_mfma_scale_f32_16x16x128_f8f6f4 v[130:133], v[24:31], v[216:223], 0, v200, v201 op_sel_hi:[0,0,0]
	v_mfma_scale_f32_16x16x128_f8f6f4 v[118:121], v[16:23], v[224:231], 0, v200, v201 op_sel_hi:[0,0,0]
	v_mfma_scale_f32_16x16x128_f8f6f4 v[114:117], v[24:31], v[224:231], 0, v200, v201 op_sel_hi:[0,0,0]
	s_setprio 0
	s_setprio 1
	v_mfma_scale_f32_16x16x128_f8f6f4 v[142:145], v[0:7], v[174:181], 0, v200, v201 op_sel_hi:[0,0,0]
	v_mfma_scale_f32_16x16x128_f8f6f4 v[138:141], v[8:15], v[174:181], 0, v200, v201 op_sel_hi:[0,0,0]
	v_mfma_scale_f32_16x16x128_f8f6f4 v[126:129], v[0:7], v[186:193], 0, v200, v201 op_sel_hi:[0,0,0]
	v_mfma_scale_f32_16x16x128_f8f6f4 v[122:125], v[8:15], v[186:193], 0, v200, v201 op_sel_hi:[0,0,0]
	v_mfma_scale_f32_16x16x128_f8f6f4 v[108:111], v[0:7], v[216:223], 0, v200, v201 op_sel_hi:[0,0,0]
	v_mfma_scale_f32_16x16x128_f8f6f4 v[104:107], v[8:15], v[216:223], 0, v200, v201 op_sel_hi:[0,0,0]
	v_mfma_scale_f32_16x16x128_f8f6f4 v[100:103], v[0:7], v[224:231], 0, v200, v201 op_sel_hi:[0,0,0]
	v_mfma_scale_f32_16x16x128_f8f6f4 v[96:99], v[8:15], v[224:231], 0, v200, v201 op_sel_hi:[0,0,0]
	s_setprio 0
	s_barrier
	s_add_i32 s29, s85, s14
	v_lshl_add_u64 v[174:175], s[96:97], 0, v[164:165]
	s_mov_b32 m0, s29
	ds_read_b128 v[186:189], v184 offset:16384
	ds_read_b128 v[190:193], v184 offset:17408
	ds_read_b128 v[216:219], v184 offset:18432
	ds_read_b128 v[220:223], v184 offset:19456
	ds_read_b128 v[224:227], v184 offset:20480
	ds_read_b128 v[228:231], v184 offset:21504
	ds_read_b128 v[232:235], v184 offset:22528
	ds_read_b128 v[236:239], v184 offset:23552
	global_load_lds_dwordx4 v[174:175], off
	s_add_i32 m0, s29, 0x2000
	s_add_u32 s30, s96, 0x20000
	v_lshl_add_u64 v[176:177], s[96:97], 0, v[168:169]
	s_addc_u32 s31, s97, 0
	s_add_i32 s28, s28, s14
	global_load_lds_dwordx4 v[176:177], off
	v_lshl_add_u64 v[178:179], s[30:31], 0, v[164:165]
	s_mov_b32 m0, s28
	v_lshl_add_u64 v[180:181], vcc, 0, v[166:167]
	global_load_lds_dwordx4 v[178:179], off
	v_lshl_add_u64 v[178:179], s[30:31], 0, v[168:169]
	s_add_i32 m0, s28, 0x2000
	s_nop 0
	global_load_lds_dwordx4 v[178:179], off
	v_lshl_add_u64 v[178:179], vcc, 0, v[162:163]
	s_mov_b32 m0, s6
	s_nop 0
	global_load_lds_dwordx4 v[178:179], off
	s_mov_b32 m0, s7
	s_nop 0
	global_load_lds_dwordx4 v[180:181], off
	s_waitcnt vmcnt(8)
	s_waitcnt lgkmcnt(0)
	s_barrier
	s_setprio 1
	s_waitcnt lgkmcnt(0)
	v_mfma_scale_f32_16x16x128_f8f6f4 v[92:95], v[16:23], v[186:193], 0, v200, v201 op_sel_hi:[0,0,0]
	v_mfma_scale_f32_16x16x128_f8f6f4 v[88:91], v[24:31], v[186:193], 0, v200, v201 op_sel_hi:[0,0,0]
	v_mfma_scale_f32_16x16x128_f8f6f4 v[84:87], v[16:23], v[216:223], 0, v200, v201 op_sel_hi:[0,0,0]
	v_mfma_scale_f32_16x16x128_f8f6f4 v[80:83], v[24:31], v[216:223], 0, v200, v201 op_sel_hi:[0,0,0]
	v_mfma_scale_f32_16x16x128_f8f6f4 v[68:71], v[16:23], v[224:231], 0, v200, v201 op_sel_hi:[0,0,0]
	v_mfma_scale_f32_16x16x128_f8f6f4 v[64:67], v[24:31], v[224:231], 0, v200, v201 op_sel_hi:[0,0,0]
	v_mfma_scale_f32_16x16x128_f8f6f4 v[52:55], v[16:23], v[232:239], 0, v200, v201 op_sel_hi:[0,0,0]
	v_mfma_scale_f32_16x16x128_f8f6f4 v[48:51], v[24:31], v[232:239], 0, v200, v201 op_sel_hi:[0,0,0]
	s_setprio 0
	s_setprio 1
	v_mfma_scale_f32_16x16x128_f8f6f4 v[76:79], v[0:7], v[186:193], 0, v200, v201 op_sel_hi:[0,0,0]
	v_mfma_scale_f32_16x16x128_f8f6f4 v[72:75], v[8:15], v[186:193], 0, v200, v201 op_sel_hi:[0,0,0]
	v_mfma_scale_f32_16x16x128_f8f6f4 v[60:63], v[0:7], v[216:223], 0, v200, v201 op_sel_hi:[0,0,0]
	v_mfma_scale_f32_16x16x128_f8f6f4 v[56:59], v[8:15], v[216:223], 0, v200, v201 op_sel_hi:[0,0,0]
	v_mfma_scale_f32_16x16x128_f8f6f4 v[44:47], v[0:7], v[224:231], 0, v200, v201 op_sel_hi:[0,0,0]
	v_mfma_scale_f32_16x16x128_f8f6f4 v[40:43], v[8:15], v[224:231], 0, v200, v201 op_sel_hi:[0,0,0]
	v_mfma_scale_f32_16x16x128_f8f6f4 v[36:39], v[0:7], v[232:239], 0, v200, v201 op_sel_hi:[0,0,0]
	v_mfma_scale_f32_16x16x128_f8f6f4 v[32:35], v[8:15], v[232:239], 0, v200, v201 op_sel_hi:[0,0,0]
	s_setprio 0
	s_barrier
	s_add_i32 s30, 0, 0x18000
	s_add_i32 s31, 0, 0x1c000
	v_add_u32_e32 v12, s30, v183
	v_add_u32_e32 v28, s31, v183
	ds_read_b128 v[0:3], v12
	ds_read_b128 v[4:7], v12 offset:1024
	ds_read_b128 v[8:11], v12 offset:2048
	ds_read_b128 v[12:15], v12 offset:3072
	ds_read_b128 v[16:19], v28
	ds_read_b128 v[20:23], v28 offset:1024
	ds_read_b128 v[24:27], v28 offset:2048
	ds_read_b128 v[28:31], v28 offset:3072
	s_add_u32 s28, vcc_lo, 0x20000
	s_addc_u32 s29, vcc_hi, 0
	s_mov_b32 m0, s86
	v_lshl_add_u64 v[194:195], s[28:29], 0, v[162:163]
	ds_read_b128 v[186:189], v184 offset:32768
	ds_read_b128 v[190:193], v184 offset:33792
	ds_read_b128 v[216:219], v184 offset:34816
	ds_read_b128 v[220:223], v184 offset:35840
	ds_read_b128 v[224:227], v184 offset:36864
	ds_read_b128 v[228:231], v184 offset:37888
	ds_read_b128 v[232:235], v184 offset:38912
	ds_read_b128 v[236:239], v184 offset:39936
	global_load_lds_dwordx4 v[194:195], off
	v_lshl_add_u64 v[194:195], s[28:29], 0, v[166:167]
	s_mov_b32 m0, s33
	s_nop 0
	global_load_lds_dwordx4 v[194:195], off
	s_waitcnt vmcnt(8)
	s_waitcnt lgkmcnt(0)
	s_barrier
	s_setprio 1
	s_waitcnt lgkmcnt(0)
	v_mfma_scale_f32_16x16x128_f8f6f4 v[158:161], v[0:7], v[186:193], v[158:161], v200, v201 op_sel_hi:[0,0,0]
	v_mfma_scale_f32_16x16x128_f8f6f4 v[154:157], v[8:15], v[186:193], v[154:157], v200, v201 op_sel_hi:[0,0,0]
	v_mfma_scale_f32_16x16x128_f8f6f4 v[150:153], v[0:7], v[216:223], v[150:153], v200, v201 op_sel_hi:[0,0,0]
	v_mfma_scale_f32_16x16x128_f8f6f4 v[146:149], v[8:15], v[216:223], v[146:149], v200, v201 op_sel_hi:[0,0,0]
	v_mfma_scale_f32_16x16x128_f8f6f4 v[134:137], v[0:7], v[224:231], v[134:137], v200, v201 op_sel_hi:[0,0,0]
	v_mfma_scale_f32_16x16x128_f8f6f4 v[130:133], v[8:15], v[224:231], v[130:133], v200, v201 op_sel_hi:[0,0,0]
	v_mfma_scale_f32_16x16x128_f8f6f4 v[118:121], v[0:7], v[232:239], v[118:121], v200, v201 op_sel_hi:[0,0,0]
	v_mfma_scale_f32_16x16x128_f8f6f4 v[114:117], v[8:15], v[232:239], v[114:117], v200, v201 op_sel_hi:[0,0,0]
	s_setprio 0
	s_setprio 1
	v_mfma_scale_f32_16x16x128_f8f6f4 v[142:145], v[16:23], v[186:193], v[142:145], v200, v201 op_sel_hi:[0,0,0]
	v_mfma_scale_f32_16x16x128_f8f6f4 v[138:141], v[24:31], v[186:193], v[138:141], v200, v201 op_sel_hi:[0,0,0]
	v_mfma_scale_f32_16x16x128_f8f6f4 v[126:129], v[16:23], v[216:223], v[126:129], v200, v201 op_sel_hi:[0,0,0]
	v_mfma_scale_f32_16x16x128_f8f6f4 v[122:125], v[24:31], v[216:223], v[122:125], v200, v201 op_sel_hi:[0,0,0]
	v_mfma_scale_f32_16x16x128_f8f6f4 v[108:111], v[16:23], v[224:231], v[108:111], v200, v201 op_sel_hi:[0,0,0]
	v_mfma_scale_f32_16x16x128_f8f6f4 v[104:107], v[24:31], v[224:231], v[104:107], v200, v201 op_sel_hi:[0,0,0]
	v_mfma_scale_f32_16x16x128_f8f6f4 v[100:103], v[16:23], v[232:239], v[100:103], v200, v201 op_sel_hi:[0,0,0]
	v_mfma_scale_f32_16x16x128_f8f6f4 v[96:99], v[24:31], v[232:239], v[96:99], v200, v201 op_sel_hi:[0,0,0]
	s_setprio 0
	s_barrier
	s_add_i32 s28, s30, s14
	v_lshl_add_u64 v[174:175], v[174:175], 0, s[56:57]
	s_mov_b32 m0, s28
	ds_read_b128 v[186:189], v184 offset:49152
	ds_read_b128 v[190:193], v184 offset:50176
	ds_read_b128 v[216:219], v184 offset:51200
	ds_read_b128 v[220:223], v184 offset:52224
	ds_read_b128 v[224:227], v184 offset:53248
	ds_read_b128 v[228:231], v184 offset:54272
	ds_read_b128 v[232:235], v184 offset:55296
	ds_read_b128 v[236:239], v184 offset:56320
	global_load_lds_dwordx4 v[174:175], off
	s_add_i32 m0, s28, 0x2000
	s_add_u32 s28, s96, 0x20080
	v_lshl_add_u64 v[174:175], v[176:177], 0, s[56:57]
	s_addc_u32 s29, s97, 0
	s_add_i32 s30, s31, s14
	global_load_lds_dwordx4 v[174:175], off
	v_lshl_add_u64 v[174:175], s[28:29], 0, v[164:165]
	s_mov_b32 m0, s30
	s_nop 0
	global_load_lds_dwordx4 v[174:175], off
	v_lshl_add_u64 v[174:175], s[28:29], 0, v[168:169]
	s_add_i32 m0, s30, 0x2000
	s_nop 0
	global_load_lds_dwordx4 v[174:175], off
	v_lshl_add_u64 v[174:175], v[178:179], 0, s[56:57]
	s_mov_b32 m0, s54
	s_nop 0
	global_load_lds_dwordx4 v[174:175], off
	v_lshl_add_u64 v[174:175], v[180:181], 0, s[56:57]
	s_mov_b32 m0, s55
	s_nop 0
	global_load_lds_dwordx4 v[174:175], off
	s_waitcnt vmcnt(8)
	s_waitcnt lgkmcnt(0)
	s_barrier
	s_setprio 1
	s_waitcnt lgkmcnt(0)
	v_mfma_scale_f32_16x16x128_f8f6f4 v[92:95], v[0:7], v[186:193], v[92:95], v200, v201 op_sel_hi:[0,0,0]
	v_mfma_scale_f32_16x16x128_f8f6f4 v[88:91], v[8:15], v[186:193], v[88:91], v200, v201 op_sel_hi:[0,0,0]
	v_mfma_scale_f32_16x16x128_f8f6f4 v[84:87], v[0:7], v[216:223], v[84:87], v200, v201 op_sel_hi:[0,0,0]
	v_mfma_scale_f32_16x16x128_f8f6f4 v[80:83], v[8:15], v[216:223], v[80:83], v200, v201 op_sel_hi:[0,0,0]
	v_mfma_scale_f32_16x16x128_f8f6f4 v[68:71], v[0:7], v[224:231], v[68:71], v200, v201 op_sel_hi:[0,0,0]
	v_mfma_scale_f32_16x16x128_f8f6f4 v[64:67], v[8:15], v[224:231], v[64:67], v200, v201 op_sel_hi:[0,0,0]
	v_mfma_scale_f32_16x16x128_f8f6f4 v[52:55], v[0:7], v[232:239], v[52:55], v200, v201 op_sel_hi:[0,0,0]
	v_mfma_scale_f32_16x16x128_f8f6f4 v[48:51], v[8:15], v[232:239], v[48:51], v200, v201 op_sel_hi:[0,0,0]
	s_setprio 0
	s_setprio 1
	v_mfma_scale_f32_16x16x128_f8f6f4 v[76:79], v[16:23], v[186:193], v[76:79], v200, v201 op_sel_hi:[0,0,0]
	v_mfma_scale_f32_16x16x128_f8f6f4 v[72:75], v[24:31], v[186:193], v[72:75], v200, v201 op_sel_hi:[0,0,0]
	v_mfma_scale_f32_16x16x128_f8f6f4 v[60:63], v[16:23], v[216:223], v[60:63], v200, v201 op_sel_hi:[0,0,0]
	v_mfma_scale_f32_16x16x128_f8f6f4 v[56:59], v[24:31], v[216:223], v[56:59], v200, v201 op_sel_hi:[0,0,0]
	v_mfma_scale_f32_16x16x128_f8f6f4 v[44:47], v[16:23], v[224:231], v[44:47], v200, v201 op_sel_hi:[0,0,0]
	v_mfma_scale_f32_16x16x128_f8f6f4 v[40:43], v[24:31], v[224:231], v[40:43], v200, v201 op_sel_hi:[0,0,0]
	v_mfma_scale_f32_16x16x128_f8f6f4 v[36:39], v[16:23], v[232:239], v[36:39], v200, v201 op_sel_hi:[0,0,0]
	v_mfma_scale_f32_16x16x128_f8f6f4 v[32:35], v[24:31], v[232:239], v[32:35], v200, v201 op_sel_hi:[0,0,0]
	s_setprio 0
	s_barrier
	s_add_i32 s84, s84, 2
	s_add_u32 s82, s82, 0x100
	s_addc_u32 s83, s83, 0
	s_add_u32 s73, s73, 0x100
	s_addc_u32 s75, s75, 0
	s_cmp_gt_u32 s84, 5
	.p2align	6

.LBB0_757:
	s_ashr_i32 s29, s4, 31
	s_mov_b32 s28, s4
	s_ashr_i32 s7, s6, 31
	s_lshl_b64 s[28:29], s[28:29], 19
	s_lshl_b64 s[30:31], s[6:7], 17
	s_add_u32 s7, s14, s28
	s_addc_u32 s28, s15, s29
	s_add_u32 s70, s7, s30
	s_addc_u32 s71, s28, s31
	s_and_b64 s[28:29], s[78:79], exec
	s_cselect_b32 s7, s71, s73
	s_cselect_b32 s37, s70, s72
	s_mov_b64 s[80:81], 0
	s_mov_b64 s[78:79], -1
	s_mov_b64 s[50:51], 0
	.p2align	6

.Lpeel_wo:
	s_add_u32 s28, s78, 0xfffc0080
	s_addc_u32 s29, s79, -1
	s_add_i32 s30, 0, 0x10000
	s_cmp_eq_u32 s84, 12
	s_cselect_b32 s83, s37, s29
	s_cselect_b32 s82, s50, s28
	v_add_u32_e32 v112, s30, v183
	s_cselect_b32 s81, s51, s77
	s_cselect_b32 s80, s65, s71
	s_add_i32 s31, 0, 0x14000
	ds_read_b128 v[130:133], v112
	ds_read_b128 v[134:137], v112 offset:1024
	ds_read_b128 v[150:153], v112 offset:2048
	ds_read_b128 v[154:157], v112 offset:3072
	v_add_u32_e32 v112, s31, v183
	ds_read_b128 v[158:161], v112
	ds_read_b128 v[162:165], v112 offset:1024
	ds_read_b128 v[166:169], v112 offset:2048
	ds_read_b128 v[170:173], v112 offset:3072
	v_lshl_add_u64 v[194:195], s[78:79], 0, v[146:147]
	s_add_i32 m0, s34, 0xc000
	ds_read_b128 v[174:177], v184
	ds_read_b128 v[178:181], v184 offset:1024
	ds_read_b128 v[186:189], v184 offset:2048
	ds_read_b128 v[190:193], v184 offset:3072
	ds_read_b128 v[206:209], v184 offset:4096
	ds_read_b128 v[210:213], v184 offset:5120
	ds_read_b128 v[216:219], v184 offset:6144
	ds_read_b128 v[220:223], v184 offset:7168
	global_load_lds_dwordx4 v[194:195], off
	v_lshl_add_u64 v[194:195], s[78:79], 0, v[148:149]
	s_add_i32 m0, s34, 0xe000
	s_nop 0
	global_load_lds_dwordx4 v[194:195], off
	s_waitcnt vmcnt(8)
	s_waitcnt lgkmcnt(0)
	s_barrier
	s_setprio 1
	s_waitcnt lgkmcnt(0)
	v_mfma_f32_16x16x32_bf16 v[126:129], v[130:133], v[174:177], 0
	v_mfma_f32_16x16x32_bf16 v[122:125], v[150:153], v[174:177], 0
	v_mfma_f32_16x16x32_bf16 v[118:121], v[130:133], v[186:189], 0
	v_mfma_f32_16x16x32_bf16 v[114:117], v[150:153], v[186:189], 0
	v_mfma_f32_16x16x32_bf16 v[108:111], v[130:133], v[206:209], 0
	v_mfma_f32_16x16x32_bf16 v[104:107], v[150:153], v[206:209], 0
	v_mfma_f32_16x16x32_bf16 v[100:103], v[130:133], v[216:219], 0
	v_mfma_f32_16x16x32_bf16 v[96:99], v[150:153], v[216:219], 0
	v_mfma_f32_16x16x32_bf16 v[126:129], v[134:137], v[178:181], v[126:129]
	v_mfma_f32_16x16x32_bf16 v[122:125], v[154:157], v[178:181], v[122:125]
	v_mfma_f32_16x16x32_bf16 v[118:121], v[134:137], v[190:193], v[118:121]
	v_mfma_f32_16x16x32_bf16 v[114:117], v[154:157], v[190:193], v[114:117]
	v_mfma_f32_16x16x32_bf16 v[108:111], v[134:137], v[210:213], v[108:111]
	v_mfma_f32_16x16x32_bf16 v[104:107], v[154:157], v[210:213], v[104:107]
	v_mfma_f32_16x16x32_bf16 v[100:103], v[134:137], v[220:223], v[100:103]
	v_mfma_f32_16x16x32_bf16 v[96:99], v[154:157], v[220:223], v[96:99]
	s_setprio 0
	s_setprio 1
	v_mfma_f32_16x16x32_bf16 v[60:63], v[158:161], v[174:177], 0
	v_mfma_f32_16x16x32_bf16 v[56:59], v[166:169], v[174:177], 0
	v_mfma_f32_16x16x32_bf16 v[52:55], v[158:161], v[186:189], 0
	v_mfma_f32_16x16x32_bf16 v[48:51], v[166:169], v[186:189], 0
	v_mfma_f32_16x16x32_bf16 v[44:47], v[158:161], v[206:209], 0
	v_mfma_f32_16x16x32_bf16 v[40:43], v[166:169], v[206:209], 0
	v_mfma_f32_16x16x32_bf16 v[36:39], v[158:161], v[216:219], 0
	v_mfma_f32_16x16x32_bf16 v[32:35], v[166:169], v[216:219], 0
	v_mfma_f32_16x16x32_bf16 v[60:63], v[162:165], v[178:181], v[60:63]
	v_mfma_f32_16x16x32_bf16 v[56:59], v[170:173], v[178:181], v[56:59]
	v_mfma_f32_16x16x32_bf16 v[52:55], v[162:165], v[190:193], v[52:55]
	v_mfma_f32_16x16x32_bf16 v[48:51], v[170:173], v[190:193], v[48:51]
	v_mfma_f32_16x16x32_bf16 v[44:47], v[162:165], v[210:213], v[44:47]
	v_mfma_f32_16x16x32_bf16 v[40:43], v[170:173], v[210:213], v[40:43]
	v_mfma_f32_16x16x32_bf16 v[36:39], v[162:165], v[220:223], v[36:39]
	v_mfma_f32_16x16x32_bf16 v[32:35], v[170:173], v[220:223], v[32:35]
	s_setprio 0
	s_barrier
	s_add_i32 s28, s30, s33
	v_lshl_add_u64 v[194:195], s[80:81], 0, v[140:141]
	s_mov_b32 m0, s28
	ds_read_b128 v[174:177], v184 offset:16384
	ds_read_b128 v[178:181], v184 offset:17408
	ds_read_b128 v[186:189], v184 offset:18432
	ds_read_b128 v[190:193], v184 offset:19456
	ds_read_b128 v[206:209], v184 offset:20480
	ds_read_b128 v[210:213], v184 offset:21504
	ds_read_b128 v[216:219], v184 offset:22528
	ds_read_b128 v[220:223], v184 offset:23552
	global_load_lds_dwordx4 v[194:195], off
	s_add_i32 m0, s28, 0x2000
	s_add_u32 s28, s80, 0x40000
	v_lshl_add_u64 v[224:225], s[80:81], 0, v[144:145]
	s_addc_u32 s29, s81, 0
	s_add_i32 s30, s31, s33
	global_load_lds_dwordx4 v[224:225], off
	v_lshl_add_u64 v[226:227], s[28:29], 0, v[140:141]
	s_mov_b32 m0, s30
	v_lshl_add_u64 v[228:229], s[82:83], 0, v[142:143]
	global_load_lds_dwordx4 v[226:227], off
	v_lshl_add_u64 v[226:227], s[28:29], 0, v[144:145]
	s_add_i32 m0, s30, 0x2000
	s_nop 0
	global_load_lds_dwordx4 v[226:227], off
	v_lshl_add_u64 v[226:227], s[82:83], 0, v[138:139]
	s_mov_b32 m0, s34
	s_nop 0
	global_load_lds_dwordx4 v[226:227], off
	s_mov_b32 m0, s54
	s_nop 0
	global_load_lds_dwordx4 v[228:229], off
	s_waitcnt vmcnt(8)
	s_waitcnt lgkmcnt(0)
	s_barrier
	s_setprio 1
	s_waitcnt lgkmcnt(0)
	v_mfma_f32_16x16x32_bf16 v[92:95], v[130:133], v[174:177], 0
	v_mfma_f32_16x16x32_bf16 v[88:91], v[150:153], v[174:177], 0
	v_mfma_f32_16x16x32_bf16 v[84:87], v[130:133], v[186:189], 0
	v_mfma_f32_16x16x32_bf16 v[80:83], v[150:153], v[186:189], 0
	v_mfma_f32_16x16x32_bf16 v[76:79], v[130:133], v[206:209], 0
	v_mfma_f32_16x16x32_bf16 v[72:75], v[150:153], v[206:209], 0
	v_mfma_f32_16x16x32_bf16 v[68:71], v[130:133], v[216:219], 0
	v_mfma_f32_16x16x32_bf16 v[64:67], v[150:153], v[216:219], 0
	v_mfma_f32_16x16x32_bf16 v[92:95], v[134:137], v[178:181], v[92:95]
	v_mfma_f32_16x16x32_bf16 v[88:91], v[154:157], v[178:181], v[88:91]
	v_mfma_f32_16x16x32_bf16 v[84:87], v[134:137], v[190:193], v[84:87]
	v_mfma_f32_16x16x32_bf16 v[80:83], v[154:157], v[190:193], v[80:83]
	v_mfma_f32_16x16x32_bf16 v[76:79], v[134:137], v[210:213], v[76:79]
	v_mfma_f32_16x16x32_bf16 v[72:75], v[154:157], v[210:213], v[72:75]
	v_mfma_f32_16x16x32_bf16 v[68:71], v[134:137], v[220:223], v[68:71]
	v_mfma_f32_16x16x32_bf16 v[64:67], v[154:157], v[220:223], v[64:67]
	s_setprio 0
	s_setprio 1
	v_mfma_f32_16x16x32_bf16 v[28:31], v[158:161], v[174:177], 0
	v_mfma_f32_16x16x32_bf16 v[24:27], v[166:169], v[174:177], 0
	v_mfma_f32_16x16x32_bf16 v[20:23], v[158:161], v[186:189], 0
	v_mfma_f32_16x16x32_bf16 v[16:19], v[166:169], v[186:189], 0
	v_mfma_f32_16x16x32_bf16 v[12:15], v[158:161], v[206:209], 0
	v_mfma_f32_16x16x32_bf16 v[8:11], v[166:169], v[206:209], 0
	v_mfma_f32_16x16x32_bf16 v[4:7], v[158:161], v[216:219], 0
	v_mfma_f32_16x16x32_bf16 v[0:3], v[166:169], v[216:219], 0
	v_mfma_f32_16x16x32_bf16 v[28:31], v[162:165], v[178:181], v[28:31]
	v_mfma_f32_16x16x32_bf16 v[24:27], v[170:173], v[178:181], v[24:27]
	v_mfma_f32_16x16x32_bf16 v[20:23], v[162:165], v[190:193], v[20:23]
	v_mfma_f32_16x16x32_bf16 v[16:19], v[170:173], v[190:193], v[16:19]
	v_mfma_f32_16x16x32_bf16 v[12:15], v[162:165], v[210:213], v[12:15]
	v_mfma_f32_16x16x32_bf16 v[8:11], v[170:173], v[210:213], v[8:11]
	v_mfma_f32_16x16x32_bf16 v[4:7], v[162:165], v[220:223], v[4:7]
	v_mfma_f32_16x16x32_bf16 v[0:3], v[170:173], v[220:223], v[0:3]
	s_setprio 0
	s_barrier
	s_add_i32 s30, 0, 0x18000
	v_add_u32_e32 v112, s30, v183
	s_add_i32 s31, 0, 0x1c000
	ds_read_b128 v[130:133], v112
	ds_read_b128 v[134:137], v112 offset:1024
	ds_read_b128 v[150:153], v112 offset:2048
	ds_read_b128 v[154:157], v112 offset:3072
	v_add_u32_e32 v112, s31, v183
	ds_read_b128 v[158:161], v112
	ds_read_b128 v[162:165], v112 offset:1024
	ds_read_b128 v[166:169], v112 offset:2048
	ds_read_b128 v[170:173], v112 offset:3072
	s_add_u32 s28, s82, 0x40000
	s_addc_u32 s29, s83, 0
	s_mov_b32 m0, s55
	v_lshl_add_u64 v[230:231], s[28:29], 0, v[138:139]
	ds_read_b128 v[174:177], v184 offset:32768
	ds_read_b128 v[178:181], v184 offset:33792
	ds_read_b128 v[186:189], v184 offset:34816
	ds_read_b128 v[190:193], v184 offset:35840
	ds_read_b128 v[206:209], v184 offset:36864
	ds_read_b128 v[210:213], v184 offset:37888
	ds_read_b128 v[216:219], v184 offset:38912
	ds_read_b128 v[220:223], v184 offset:39936
	global_load_lds_dwordx4 v[230:231], off
	v_lshl_add_u64 v[230:231], s[28:29], 0, v[142:143]
	s_mov_b32 m0, s58
	s_nop 0
	global_load_lds_dwordx4 v[230:231], off
	s_waitcnt vmcnt(8)
	s_waitcnt lgkmcnt(0)
	s_barrier
	s_setprio 1
	s_waitcnt lgkmcnt(0)
	v_mfma_f32_16x16x32_bf16 v[126:129], v[130:133], v[174:177], v[126:129]
	v_mfma_f32_16x16x32_bf16 v[122:125], v[150:153], v[174:177], v[122:125]
	v_mfma_f32_16x16x32_bf16 v[118:121], v[130:133], v[186:189], v[118:121]
	v_mfma_f32_16x16x32_bf16 v[114:117], v[150:153], v[186:189], v[114:117]
	v_mfma_f32_16x16x32_bf16 v[108:111], v[130:133], v[206:209], v[108:111]
	v_mfma_f32_16x16x32_bf16 v[104:107], v[150:153], v[206:209], v[104:107]
	v_mfma_f32_16x16x32_bf16 v[100:103], v[130:133], v[216:219], v[100:103]
	v_mfma_f32_16x16x32_bf16 v[96:99], v[150:153], v[216:219], v[96:99]
	v_mfma_f32_16x16x32_bf16 v[126:129], v[134:137], v[178:181], v[126:129]
	v_mfma_f32_16x16x32_bf16 v[122:125], v[154:157], v[178:181], v[122:125]
	v_mfma_f32_16x16x32_bf16 v[118:121], v[134:137], v[190:193], v[118:121]
	v_mfma_f32_16x16x32_bf16 v[114:117], v[154:157], v[190:193], v[114:117]
	v_mfma_f32_16x16x32_bf16 v[108:111], v[134:137], v[210:213], v[108:111]
	v_mfma_f32_16x16x32_bf16 v[104:107], v[154:157], v[210:213], v[104:107]
	v_mfma_f32_16x16x32_bf16 v[100:103], v[134:137], v[220:223], v[100:103]
	v_mfma_f32_16x16x32_bf16 v[96:99], v[154:157], v[220:223], v[96:99]
	s_setprio 0
	s_setprio 1
	v_mfma_f32_16x16x32_bf16 v[60:63], v[158:161], v[174:177], v[60:63]
	v_mfma_f32_16x16x32_bf16 v[56:59], v[166:169], v[174:177], v[56:59]
	v_mfma_f32_16x16x32_bf16 v[52:55], v[158:161], v[186:189], v[52:55]
	v_mfma_f32_16x16x32_bf16 v[48:51], v[166:169], v[186:189], v[48:51]
	v_mfma_f32_16x16x32_bf16 v[44:47], v[158:161], v[206:209], v[44:47]
	v_mfma_f32_16x16x32_bf16 v[40:43], v[166:169], v[206:209], v[40:43]
	v_mfma_f32_16x16x32_bf16 v[36:39], v[158:161], v[216:219], v[36:39]
	v_mfma_f32_16x16x32_bf16 v[32:35], v[166:169], v[216:219], v[32:35]
	v_mfma_f32_16x16x32_bf16 v[60:63], v[162:165], v[178:181], v[60:63]
	v_mfma_f32_16x16x32_bf16 v[56:59], v[170:173], v[178:181], v[56:59]
	v_mfma_f32_16x16x32_bf16 v[52:55], v[162:165], v[190:193], v[52:55]
	v_mfma_f32_16x16x32_bf16 v[48:51], v[170:173], v[190:193], v[48:51]
	v_mfma_f32_16x16x32_bf16 v[44:47], v[162:165], v[210:213], v[44:47]
	v_mfma_f32_16x16x32_bf16 v[40:43], v[170:173], v[210:213], v[40:43]
	v_mfma_f32_16x16x32_bf16 v[36:39], v[162:165], v[220:223], v[36:39]
	v_mfma_f32_16x16x32_bf16 v[32:35], v[170:173], v[220:223], v[32:35]
	s_setprio 0
	s_barrier
	s_add_i32 s28, s30, s33
	v_lshl_add_u64 v[194:195], v[194:195], 0, s[56:57]
	s_mov_b32 m0, s28
	ds_read_b128 v[174:177], v184 offset:49152
	ds_read_b128 v[178:181], v184 offset:50176
	ds_read_b128 v[186:189], v184 offset:51200
	ds_read_b128 v[190:193], v184 offset:52224
	ds_read_b128 v[206:209], v184 offset:53248
	ds_read_b128 v[210:213], v184 offset:54272
	ds_read_b128 v[216:219], v184 offset:55296
	ds_read_b128 v[220:223], v184 offset:56320
	global_load_lds_dwordx4 v[194:195], off
	s_add_i32 m0, s28, 0x2000
	s_add_u32 s28, s80, 0x40080
	v_lshl_add_u64 v[194:195], v[224:225], 0, s[56:57]
	s_addc_u32 s29, s81, 0
	s_add_i32 s30, s31, s33
	global_load_lds_dwordx4 v[194:195], off
	v_lshl_add_u64 v[194:195], s[28:29], 0, v[140:141]
	s_mov_b32 m0, s30
	s_nop 0
	global_load_lds_dwordx4 v[194:195], off
	v_lshl_add_u64 v[194:195], s[28:29], 0, v[144:145]
	s_add_i32 m0, s30, 0x2000
	s_nop 0
	global_load_lds_dwordx4 v[194:195], off
	v_lshl_add_u64 v[194:195], v[226:227], 0, s[56:57]
	s_mov_b32 m0, s86
	s_nop 0
	global_load_lds_dwordx4 v[194:195], off
	v_lshl_add_u64 v[194:195], v[228:229], 0, s[56:57]
	s_mov_b32 m0, s96
	s_nop 0
	global_load_lds_dwordx4 v[194:195], off
	s_waitcnt vmcnt(8)
	s_waitcnt lgkmcnt(0)
	s_barrier
	s_setprio 1
	s_waitcnt lgkmcnt(0)
	v_mfma_f32_16x16x32_bf16 v[92:95], v[130:133], v[174:177], v[92:95]
	v_mfma_f32_16x16x32_bf16 v[88:91], v[150:153], v[174:177], v[88:91]
	v_mfma_f32_16x16x32_bf16 v[84:87], v[130:133], v[186:189], v[84:87]
	v_mfma_f32_16x16x32_bf16 v[80:83], v[150:153], v[186:189], v[80:83]
	v_mfma_f32_16x16x32_bf16 v[76:79], v[130:133], v[206:209], v[76:79]
	v_mfma_f32_16x16x32_bf16 v[72:75], v[150:153], v[206:209], v[72:75]
	v_mfma_f32_16x16x32_bf16 v[68:71], v[130:133], v[216:219], v[68:71]
	v_mfma_f32_16x16x32_bf16 v[64:67], v[150:153], v[216:219], v[64:67]
	v_mfma_f32_16x16x32_bf16 v[92:95], v[134:137], v[178:181], v[92:95]
	v_mfma_f32_16x16x32_bf16 v[88:91], v[154:157], v[178:181], v[88:91]
	v_mfma_f32_16x16x32_bf16 v[84:87], v[134:137], v[190:193], v[84:87]
	v_mfma_f32_16x16x32_bf16 v[80:83], v[154:157], v[190:193], v[80:83]
	v_mfma_f32_16x16x32_bf16 v[76:79], v[134:137], v[210:213], v[76:79]
	v_mfma_f32_16x16x32_bf16 v[72:75], v[154:157], v[210:213], v[72:75]
	v_mfma_f32_16x16x32_bf16 v[68:71], v[134:137], v[220:223], v[68:71]
	v_mfma_f32_16x16x32_bf16 v[64:67], v[154:157], v[220:223], v[64:67]
	s_setprio 0
	s_setprio 1
	v_mfma_f32_16x16x32_bf16 v[28:31], v[158:161], v[174:177], v[28:31]
	v_mfma_f32_16x16x32_bf16 v[24:27], v[166:169], v[174:177], v[24:27]
	v_mfma_f32_16x16x32_bf16 v[20:23], v[158:161], v[186:189], v[20:23]
	v_mfma_f32_16x16x32_bf16 v[16:19], v[166:169], v[186:189], v[16:19]
	v_mfma_f32_16x16x32_bf16 v[12:15], v[158:161], v[206:209], v[12:15]
	v_mfma_f32_16x16x32_bf16 v[8:11], v[166:169], v[206:209], v[8:11]
	v_mfma_f32_16x16x32_bf16 v[4:7], v[158:161], v[216:219], v[4:7]
	v_mfma_f32_16x16x32_bf16 v[0:3], v[166:169], v[216:219], v[0:3]
	v_mfma_f32_16x16x32_bf16 v[28:31], v[162:165], v[178:181], v[28:31]
	v_mfma_f32_16x16x32_bf16 v[24:27], v[170:173], v[178:181], v[24:27]
	v_mfma_f32_16x16x32_bf16 v[20:23], v[162:165], v[190:193], v[20:23]
	v_mfma_f32_16x16x32_bf16 v[16:19], v[170:173], v[190:193], v[16:19]
	v_mfma_f32_16x16x32_bf16 v[12:15], v[162:165], v[210:213], v[12:15]
	v_mfma_f32_16x16x32_bf16 v[8:11], v[170:173], v[210:213], v[8:11]
	v_mfma_f32_16x16x32_bf16 v[4:7], v[162:165], v[220:223], v[4:7]
	v_mfma_f32_16x16x32_bf16 v[0:3], v[170:173], v[220:223], v[0:3]
	s_setprio 0
	s_barrier
	s_add_i32 s84, s84, 2
	s_add_u32 s78, s78, 0x100
	s_addc_u32 s79, s79, 0
	s_add_u32 s71, s71, 0x100
	s_addc_u32 s77, s77, 0
	s_cmp_gt_u32 s84, 13
	.p2align	6

.LBB0_1089:
	s_add_u32 s30, s94, s72
	s_addc_u32 s31, s95, s73
	s_add_u32 s45, s30, 0x28dd9100
	s_addc_u32 s55, s31, 0
	s_and_b64 s[30:31], s[40:41], exec
	s_cselect_b32 s77, s91, s55
	s_cselect_b32 s76, s90, s45
	s_add_u32 s45, s37, s72
	s_addc_u32 s55, s47, s73
	s_and_b64 s[30:31], s[40:41], exec
	s_cselect_b32 s75, s65, s55
	s_cselect_b32 s74, s64, s45
	s_add_i32 s55, 0, 0x10000
	s_add_i32 s58, 0, 0x14000
	v_add_u32_e32 v0, s55, v193
	v_add_u32_e32 v12, s58, v193
	ds_read_b128 v[16:19], v0
	ds_read_b128 v[20:23], v0 offset:1024
	ds_read_b128 v[24:27], v0 offset:2048
	ds_read_b128 v[28:31], v0 offset:3072
	ds_read_b128 v[0:3], v12
	ds_read_b128 v[4:7], v12 offset:1024
	ds_read_b128 v[8:11], v12 offset:2048
	ds_read_b128 v[12:15], v12 offset:3072
	v_lshl_add_u64 v[206:207], v[178:179], 0, s[72:73]
	s_add_i32 m0, s7, 0xc000
	ds_read_b128 v[180:183], v169
	ds_read_b128 v[184:187], v169 offset:1024
	ds_read_b128 v[224:227], v169 offset:2048
	ds_read_b128 v[228:231], v169 offset:3072
	ds_read_b128 v[232:235], v169 offset:4096
	ds_read_b128 v[236:239], v169 offset:5120
	ds_read_b128 v[240:243], v169 offset:6144
	ds_read_b128 v[244:247], v169 offset:7168
	global_load_lds_dwordx4 v[206:207], off
	v_lshl_add_u64 v[206:207], v[176:177], 0, s[72:73]
	s_add_i32 m0, s7, 0xe000
	s_nop 0
	global_load_lds_dwordx4 v[206:207], off
	s_waitcnt vmcnt(8)
	s_waitcnt lgkmcnt(0)
	s_barrier
	s_setprio 1
	s_waitcnt lgkmcnt(0)
	v_mfma_scale_f32_16x16x128_f8f6f4 v[158:161], v[16:23], v[180:187], v[158:161], v200, v201 op_sel_hi:[0,0,0]
	v_mfma_scale_f32_16x16x128_f8f6f4 v[150:153], v[24:31], v[180:187], v[150:153], v200, v201 op_sel_hi:[0,0,0]
	v_mfma_scale_f32_16x16x128_f8f6f4 v[142:145], v[16:23], v[224:231], v[142:145], v200, v201 op_sel_hi:[0,0,0]
	v_mfma_scale_f32_16x16x128_f8f6f4 v[134:137], v[24:31], v[224:231], v[134:137], v200, v201 op_sel_hi:[0,0,0]
	v_mfma_scale_f32_16x16x128_f8f6f4 v[126:129], v[16:23], v[232:239], v[126:129], v200, v201 op_sel_hi:[0,0,0]
	v_mfma_scale_f32_16x16x128_f8f6f4 v[118:121], v[24:31], v[232:239], v[118:121], v200, v201 op_sel_hi:[0,0,0]
	v_mfma_scale_f32_16x16x128_f8f6f4 v[108:111], v[16:23], v[240:247], v[108:111], v200, v201 op_sel_hi:[0,0,0]
	v_mfma_scale_f32_16x16x128_f8f6f4 v[100:103], v[24:31], v[240:247], v[100:103], v200, v201 op_sel_hi:[0,0,0]
	s_setprio 0
	s_setprio 1
	v_mfma_scale_f32_16x16x128_f8f6f4 v[154:157], v[0:7], v[180:187], v[154:157], v200, v201 op_sel_hi:[0,0,0]
	v_mfma_scale_f32_16x16x128_f8f6f4 v[146:149], v[8:15], v[180:187], v[146:149], v200, v201 op_sel_hi:[0,0,0]
	v_mfma_scale_f32_16x16x128_f8f6f4 v[138:141], v[0:7], v[224:231], v[138:141], v200, v201 op_sel_hi:[0,0,0]
	v_mfma_scale_f32_16x16x128_f8f6f4 v[130:133], v[8:15], v[224:231], v[130:133], v200, v201 op_sel_hi:[0,0,0]
	v_mfma_scale_f32_16x16x128_f8f6f4 v[122:125], v[0:7], v[232:239], v[122:125], v200, v201 op_sel_hi:[0,0,0]
	v_mfma_scale_f32_16x16x128_f8f6f4 v[114:117], v[8:15], v[232:239], v[114:117], v200, v201 op_sel_hi:[0,0,0]
	v_mfma_scale_f32_16x16x128_f8f6f4 v[104:107], v[0:7], v[240:247], v[104:107], v200, v201 op_sel_hi:[0,0,0]
	v_mfma_scale_f32_16x16x128_f8f6f4 v[96:99], v[8:15], v[240:247], v[96:99], v200, v201 op_sel_hi:[0,0,0]
	s_setprio 0
	s_barrier
	s_add_i32 s30, s55, s14
	v_lshl_add_u64 v[180:181], s[74:75], 0, v[164:165]
	s_mov_b32 m0, s30
	ds_read_b128 v[224:227], v169 offset:16384
	ds_read_b128 v[228:231], v169 offset:17408
	ds_read_b128 v[232:235], v169 offset:18432
	ds_read_b128 v[236:239], v169 offset:19456
	ds_read_b128 v[240:243], v169 offset:20480
	ds_read_b128 v[244:247], v169 offset:21504
	ds_read_b128 v[206:209], v169 offset:22528
	ds_read_b128 v[210:213], v169 offset:23552
	global_load_lds_dwordx4 v[180:181], off
	s_add_i32 m0, s30, 0x2000
	s_add_u32 s30, s74, 0x20000
	v_lshl_add_u64 v[182:183], s[74:75], 0, v[162:163]
	s_addc_u32 s31, s75, 0
	s_add_i32 s45, s58, s14
	global_load_lds_dwordx4 v[182:183], off
	v_lshl_add_u64 v[184:185], s[30:31], 0, v[164:165]
	s_mov_b32 m0, s45
	v_cndmask_b32_e64 v112, v168, v173, s[40:41]
	global_load_lds_dwordx4 v[184:185], off
	v_lshl_add_u64 v[184:185], s[30:31], 0, v[162:163]
	s_add_i32 m0, s45, 0x2000
	s_nop 0
	global_load_lds_dwordx4 v[184:185], off
	s_mov_b32 m0, s7
	v_lshl_add_u64 v[184:185], s[76:77], 0, v[112:113]
	global_load_lds_dwordx4 v112, s[76:77]
	v_cndmask_b32_e64 v112, v170, v175, s[40:41]
	s_mov_b32 m0, s33
	v_lshl_add_u64 v[186:187], s[76:77], 0, v[112:113]
	global_load_lds_dwordx4 v112, s[76:77]
	s_waitcnt vmcnt(8)
	s_waitcnt lgkmcnt(0)
	s_barrier
	s_setprio 1
	s_waitcnt lgkmcnt(0)
	v_mfma_scale_f32_16x16x128_f8f6f4 v[92:95], v[16:23], v[224:231], v[92:95], v200, v201 op_sel_hi:[0,0,0]
	v_mfma_scale_f32_16x16x128_f8f6f4 v[84:87], v[24:31], v[224:231], v[84:87], v200, v201 op_sel_hi:[0,0,0]
	v_mfma_scale_f32_16x16x128_f8f6f4 v[76:79], v[16:23], v[232:239], v[76:79], v200, v201 op_sel_hi:[0,0,0]
	v_mfma_scale_f32_16x16x128_f8f6f4 v[68:71], v[24:31], v[232:239], v[68:71], v200, v201 op_sel_hi:[0,0,0]
	v_mfma_scale_f32_16x16x128_f8f6f4 v[60:63], v[16:23], v[240:247], v[60:63], v200, v201 op_sel_hi:[0,0,0]
	v_mfma_scale_f32_16x16x128_f8f6f4 v[52:55], v[24:31], v[240:247], v[52:55], v200, v201 op_sel_hi:[0,0,0]
	v_mfma_scale_f32_16x16x128_f8f6f4 v[44:47], v[16:23], v[206:213], v[44:47], v200, v201 op_sel_hi:[0,0,0]
	v_mfma_scale_f32_16x16x128_f8f6f4 v[36:39], v[24:31], v[206:213], v[36:39], v200, v201 op_sel_hi:[0,0,0]
	s_setprio 0
	s_setprio 1
	v_mfma_scale_f32_16x16x128_f8f6f4 v[88:91], v[0:7], v[224:231], v[88:91], v200, v201 op_sel_hi:[0,0,0]
	v_mfma_scale_f32_16x16x128_f8f6f4 v[80:83], v[8:15], v[224:231], v[80:83], v200, v201 op_sel_hi:[0,0,0]
	v_mfma_scale_f32_16x16x128_f8f6f4 v[72:75], v[0:7], v[232:239], v[72:75], v200, v201 op_sel_hi:[0,0,0]
	v_mfma_scale_f32_16x16x128_f8f6f4 v[64:67], v[8:15], v[232:239], v[64:67], v200, v201 op_sel_hi:[0,0,0]
	v_mfma_scale_f32_16x16x128_f8f6f4 v[56:59], v[0:7], v[240:247], v[56:59], v200, v201 op_sel_hi:[0,0,0]
	v_mfma_scale_f32_16x16x128_f8f6f4 v[48:51], v[8:15], v[240:247], v[48:51], v200, v201 op_sel_hi:[0,0,0]
	v_mfma_scale_f32_16x16x128_f8f6f4 v[40:43], v[0:7], v[206:213], v[40:43], v200, v201 op_sel_hi:[0,0,0]
	v_mfma_scale_f32_16x16x128_f8f6f4 v[32:35], v[8:15], v[206:213], v[32:35], v200, v201 op_sel_hi:[0,0,0]
	s_setprio 0
	s_barrier
	s_add_i32 s30, 0, 0x18000
	s_add_i32 s45, 0, 0x1c000
	v_add_u32_e32 v12, s30, v193
	v_add_u32_e32 v28, s45, v193
	ds_read_b128 v[0:3], v12
	ds_read_b128 v[4:7], v12 offset:1024
	ds_read_b128 v[8:11], v12 offset:2048
	ds_read_b128 v[12:15], v12 offset:3072
	ds_read_b128 v[16:19], v28
	ds_read_b128 v[20:23], v28 offset:1024
	ds_read_b128 v[24:27], v28 offset:2048
	ds_read_b128 v[28:31], v28 offset:3072
	s_mov_b32 m0, s34
	v_cndmask_b32_e64 v112, v172, v217, s[40:41]
	ds_read_b128 v[206:209], v169 offset:32768
	ds_read_b128 v[210:213], v169 offset:33792
	ds_read_b128 v[224:227], v169 offset:34816
	ds_read_b128 v[228:231], v169 offset:35840
	ds_read_b128 v[232:235], v169 offset:36864
	ds_read_b128 v[236:239], v169 offset:37888
	ds_read_b128 v[240:243], v169 offset:38912
	ds_read_b128 v[244:247], v169 offset:39936
	global_load_lds_dwordx4 v112, s[76:77]
	v_cndmask_b32_e64 v112, v174, v218, s[40:41]
	s_mov_b32 m0, s50
	s_nop 0
	global_load_lds_dwordx4 v112, s[76:77]
	s_waitcnt vmcnt(8)
	s_waitcnt lgkmcnt(0)
	s_barrier
	s_setprio 1
	s_waitcnt lgkmcnt(0)
	v_mfma_scale_f32_16x16x128_f8f6f4 v[158:161], v[0:7], v[206:213], v[158:161], v200, v201 op_sel_hi:[0,0,0]
	v_mfma_scale_f32_16x16x128_f8f6f4 v[150:153], v[8:15], v[206:213], v[150:153], v200, v201 op_sel_hi:[0,0,0]
	v_mfma_scale_f32_16x16x128_f8f6f4 v[142:145], v[0:7], v[224:231], v[142:145], v200, v201 op_sel_hi:[0,0,0]
	v_mfma_scale_f32_16x16x128_f8f6f4 v[134:137], v[8:15], v[224:231], v[134:137], v200, v201 op_sel_hi:[0,0,0]
	v_mfma_scale_f32_16x16x128_f8f6f4 v[126:129], v[0:7], v[232:239], v[126:129], v200, v201 op_sel_hi:[0,0,0]
	v_mfma_scale_f32_16x16x128_f8f6f4 v[118:121], v[8:15], v[232:239], v[118:121], v200, v201 op_sel_hi:[0,0,0]
	v_mfma_scale_f32_16x16x128_f8f6f4 v[108:111], v[0:7], v[240:247], v[108:111], v200, v201 op_sel_hi:[0,0,0]
	v_mfma_scale_f32_16x16x128_f8f6f4 v[100:103], v[8:15], v[240:247], v[100:103], v200, v201 op_sel_hi:[0,0,0]
	s_setprio 0
	s_setprio 1
	v_mfma_scale_f32_16x16x128_f8f6f4 v[154:157], v[16:23], v[206:213], v[154:157], v200, v201 op_sel_hi:[0,0,0]
	v_mfma_scale_f32_16x16x128_f8f6f4 v[146:149], v[24:31], v[206:213], v[146:149], v200, v201 op_sel_hi:[0,0,0]
	v_mfma_scale_f32_16x16x128_f8f6f4 v[138:141], v[16:23], v[224:231], v[138:141], v200, v201 op_sel_hi:[0,0,0]
	v_mfma_scale_f32_16x16x128_f8f6f4 v[130:133], v[24:31], v[224:231], v[130:133], v200, v201 op_sel_hi:[0,0,0]
	v_mfma_scale_f32_16x16x128_f8f6f4 v[122:125], v[16:23], v[232:239], v[122:125], v200, v201 op_sel_hi:[0,0,0]
	v_mfma_scale_f32_16x16x128_f8f6f4 v[114:117], v[24:31], v[232:239], v[114:117], v200, v201 op_sel_hi:[0,0,0]
	v_mfma_scale_f32_16x16x128_f8f6f4 v[104:107], v[16:23], v[240:247], v[104:107], v200, v201 op_sel_hi:[0,0,0]
	v_mfma_scale_f32_16x16x128_f8f6f4 v[96:99], v[24:31], v[240:247], v[96:99], v200, v201 op_sel_hi:[0,0,0]
	s_setprio 0
	s_barrier
	s_add_i32 s30, s30, s14
	v_lshl_add_u64 v[180:181], v[180:181], 0, s[56:57]
	s_mov_b32 m0, s30
	ds_read_b128 v[206:209], v169 offset:49152
	ds_read_b128 v[210:213], v169 offset:50176
	ds_read_b128 v[224:227], v169 offset:51200
	ds_read_b128 v[228:231], v169 offset:52224
	ds_read_b128 v[232:235], v169 offset:53248
	ds_read_b128 v[236:239], v169 offset:54272
	ds_read_b128 v[240:243], v169 offset:55296
	ds_read_b128 v[244:247], v169 offset:56320
	global_load_lds_dwordx4 v[180:181], off
	s_add_i32 m0, s30, 0x2000
	s_add_u32 s30, s74, 0x20080
	v_lshl_add_u64 v[180:181], v[182:183], 0, s[56:57]
	s_addc_u32 s31, s75, 0
	s_add_i32 s40, s45, s14
	global_load_lds_dwordx4 v[180:181], off
	v_lshl_add_u64 v[180:181], s[30:31], 0, v[164:165]
	s_mov_b32 m0, s40
	s_nop 0
	global_load_lds_dwordx4 v[180:181], off
	v_lshl_add_u64 v[180:181], s[30:31], 0, v[162:163]
	s_add_i32 m0, s40, 0x2000
	s_nop 0
	global_load_lds_dwordx4 v[180:181], off
	v_lshl_add_u64 v[180:181], v[184:185], 0, s[56:57]
	s_mov_b32 m0, s4
	s_nop 0
	global_load_lds_dwordx4 v[180:181], off
	v_lshl_add_u64 v[180:181], v[186:187], 0, s[56:57]
	s_mov_b32 m0, s51
	s_nop 0
	global_load_lds_dwordx4 v[180:181], off
	s_waitcnt vmcnt(8)
	s_waitcnt lgkmcnt(0)
	s_barrier
	s_setprio 1
	s_waitcnt lgkmcnt(0)
	v_mfma_scale_f32_16x16x128_f8f6f4 v[92:95], v[0:7], v[206:213], v[92:95], v200, v201 op_sel_hi:[0,0,0]
	v_mfma_scale_f32_16x16x128_f8f6f4 v[84:87], v[8:15], v[206:213], v[84:87], v200, v201 op_sel_hi:[0,0,0]
	v_mfma_scale_f32_16x16x128_f8f6f4 v[76:79], v[0:7], v[224:231], v[76:79], v200, v201 op_sel_hi:[0,0,0]
	v_mfma_scale_f32_16x16x128_f8f6f4 v[68:71], v[8:15], v[224:231], v[68:71], v200, v201 op_sel_hi:[0,0,0]
	v_mfma_scale_f32_16x16x128_f8f6f4 v[60:63], v[0:7], v[232:239], v[60:63], v200, v201 op_sel_hi:[0,0,0]
	v_mfma_scale_f32_16x16x128_f8f6f4 v[52:55], v[8:15], v[232:239], v[52:55], v200, v201 op_sel_hi:[0,0,0]
	v_mfma_scale_f32_16x16x128_f8f6f4 v[44:47], v[0:7], v[240:247], v[44:47], v200, v201 op_sel_hi:[0,0,0]
	v_mfma_scale_f32_16x16x128_f8f6f4 v[36:39], v[8:15], v[240:247], v[36:39], v200, v201 op_sel_hi:[0,0,0]
	s_setprio 0
	s_setprio 1
	v_mfma_scale_f32_16x16x128_f8f6f4 v[88:91], v[16:23], v[206:213], v[88:91], v200, v201 op_sel_hi:[0,0,0]
	v_mfma_scale_f32_16x16x128_f8f6f4 v[80:83], v[24:31], v[206:213], v[80:83], v200, v201 op_sel_hi:[0,0,0]
	v_mfma_scale_f32_16x16x128_f8f6f4 v[72:75], v[16:23], v[224:231], v[72:75], v200, v201 op_sel_hi:[0,0,0]
	v_mfma_scale_f32_16x16x128_f8f6f4 v[64:67], v[24:31], v[224:231], v[64:67], v200, v201 op_sel_hi:[0,0,0]
	v_mfma_scale_f32_16x16x128_f8f6f4 v[56:59], v[16:23], v[232:239], v[56:59], v200, v201 op_sel_hi:[0,0,0]
	v_mfma_scale_f32_16x16x128_f8f6f4 v[48:51], v[24:31], v[232:239], v[48:51], v200, v201 op_sel_hi:[0,0,0]
	v_mfma_scale_f32_16x16x128_f8f6f4 v[40:43], v[16:23], v[240:247], v[40:43], v200, v201 op_sel_hi:[0,0,0]
	v_mfma_scale_f32_16x16x128_f8f6f4 v[32:35], v[24:31], v[240:247], v[32:35], v200, v201 op_sel_hi:[0,0,0]
	s_setprio 0
	s_barrier
	s_add_i32 s49, s49, 2
	s_add_u32 s72, s72, 0x100
	s_addc_u32 s73, s73, 0
	s_cmp_gt_u32 s49, 5
	s_cbranch_scc1 .LBB0_1092
	.p2align	6

.Lpeel_down:
	s_add_u32 s30, s72, 0xfffe0080
	s_addc_u32 s31, s73, -1
	s_add_i32 s51, 0, 0x10000
	s_cmp_eq_u32 s50, 4
	s_cselect_b32 s77, s27, s31
	s_cselect_b32 s76, s37, s30
	s_cselect_b32 s75, s65, s49
	s_cselect_b32 s74, s64, s47
	s_add_i32 s58, 0, 0x14000
	v_add_u32_e32 v0, s51, v183
	v_add_u32_e32 v12, s58, v183
	ds_read_b128 v[16:19], v0
	ds_read_b128 v[20:23], v0 offset:1024
	ds_read_b128 v[24:27], v0 offset:2048
	ds_read_b128 v[28:31], v0 offset:3072
	ds_read_b128 v[0:3], v12
	ds_read_b128 v[4:7], v12 offset:1024
	ds_read_b128 v[8:11], v12 offset:2048
	ds_read_b128 v[12:15], v12 offset:3072
	v_lshl_add_u64 v[194:195], s[72:73], 0, v[168:169]
	s_add_i32 m0, s7, 0xc000
	ds_read_b128 v[174:177], v184
	ds_read_b128 v[178:181], v184 offset:1024
	ds_read_b128 v[186:189], v184 offset:2048
	ds_read_b128 v[190:193], v184 offset:3072
	ds_read_b128 v[206:209], v184 offset:4096
	ds_read_b128 v[210:213], v184 offset:5120
	ds_read_b128 v[216:219], v184 offset:6144
	ds_read_b128 v[220:223], v184 offset:7168
	global_load_lds_dwordx4 v[194:195], off
	v_lshl_add_u64 v[194:195], s[72:73], 0, v[170:171]
	s_add_i32 m0, s7, 0xe000
	s_nop 0
	global_load_lds_dwordx4 v[194:195], off
	s_waitcnt vmcnt(8)
	s_waitcnt lgkmcnt(0)
	s_barrier
	s_setprio 1
	s_waitcnt lgkmcnt(0)
	v_mfma_scale_f32_16x16x128_f8f6f4 v[158:161], v[16:23], v[174:181], 0, v200, v201 op_sel_hi:[0,0,0]
	v_mfma_scale_f32_16x16x128_f8f6f4 v[154:157], v[24:31], v[174:181], 0, v200, v201 op_sel_hi:[0,0,0]
	v_mfma_scale_f32_16x16x128_f8f6f4 v[142:145], v[16:23], v[186:193], 0, v200, v201 op_sel_hi:[0,0,0]
	v_mfma_scale_f32_16x16x128_f8f6f4 v[138:141], v[24:31], v[186:193], 0, v200, v201 op_sel_hi:[0,0,0]
	v_mfma_scale_f32_16x16x128_f8f6f4 v[126:129], v[16:23], v[206:213], 0, v200, v201 op_sel_hi:[0,0,0]
	v_mfma_scale_f32_16x16x128_f8f6f4 v[122:125], v[24:31], v[206:213], 0, v200, v201 op_sel_hi:[0,0,0]
	v_mfma_scale_f32_16x16x128_f8f6f4 v[108:111], v[16:23], v[216:223], 0, v200, v201 op_sel_hi:[0,0,0]
	v_mfma_scale_f32_16x16x128_f8f6f4 v[104:107], v[24:31], v[216:223], 0, v200, v201 op_sel_hi:[0,0,0]
	s_setprio 0
	s_setprio 1
	v_mfma_scale_f32_16x16x128_f8f6f4 v[150:153], v[0:7], v[174:181], 0, v200, v201 op_sel_hi:[0,0,0]
	v_mfma_scale_f32_16x16x128_f8f6f4 v[146:149], v[8:15], v[174:181], 0, v200, v201 op_sel_hi:[0,0,0]
	v_mfma_scale_f32_16x16x128_f8f6f4 v[134:137], v[0:7], v[186:193], 0, v200, v201 op_sel_hi:[0,0,0]
	v_mfma_scale_f32_16x16x128_f8f6f4 v[130:133], v[8:15], v[186:193], 0, v200, v201 op_sel_hi:[0,0,0]
	v_mfma_scale_f32_16x16x128_f8f6f4 v[118:121], v[0:7], v[206:213], 0, v200, v201 op_sel_hi:[0,0,0]
	v_mfma_scale_f32_16x16x128_f8f6f4 v[114:117], v[8:15], v[206:213], 0, v200, v201 op_sel_hi:[0,0,0]
	v_mfma_scale_f32_16x16x128_f8f6f4 v[100:103], v[0:7], v[216:223], 0, v200, v201 op_sel_hi:[0,0,0]
	v_mfma_scale_f32_16x16x128_f8f6f4 v[96:99], v[8:15], v[216:223], 0, v200, v201 op_sel_hi:[0,0,0]
	s_setprio 0
	s_barrier
	s_add_i32 s30, s51, s14
	v_lshl_add_u64 v[174:175], s[74:75], 0, v[112:113]
	s_mov_b32 m0, s30
	ds_read_b128 v[186:189], v184 offset:16384
	ds_read_b128 v[190:193], v184 offset:17408
	ds_read_b128 v[206:209], v184 offset:18432
	ds_read_b128 v[210:213], v184 offset:19456
	ds_read_b128 v[216:219], v184 offset:20480
	ds_read_b128 v[220:223], v184 offset:21504
	ds_read_b128 v[224:227], v184 offset:22528
	ds_read_b128 v[228:231], v184 offset:23552
	global_load_lds_dwordx4 v[174:175], off
	s_add_i32 m0, s30, 0x2000
	s_add_u32 s30, s74, 0x20000
	v_lshl_add_u64 v[176:177], s[74:75], 0, v[162:163]
	s_addc_u32 s31, s75, 0
	s_add_i32 s45, s58, s14
	global_load_lds_dwordx4 v[176:177], off
	v_lshl_add_u64 v[178:179], s[30:31], 0, v[112:113]
	s_mov_b32 m0, s45
	v_lshl_add_u64 v[180:181], s[76:77], 0, v[164:165]
	global_load_lds_dwordx4 v[178:179], off
	v_lshl_add_u64 v[178:179], s[30:31], 0, v[162:163]
	s_add_i32 m0, s45, 0x2000
	s_nop 0
	global_load_lds_dwordx4 v[178:179], off
	v_lshl_add_u64 v[178:179], s[76:77], 0, v[166:167]
	s_mov_b32 m0, s7
	s_nop 0
	global_load_lds_dwordx4 v[178:179], off
	s_mov_b32 m0, s25
	s_nop 0
	global_load_lds_dwordx4 v[180:181], off
	s_waitcnt vmcnt(8)
	s_waitcnt lgkmcnt(0)
	s_barrier
	s_setprio 1
	s_waitcnt lgkmcnt(0)
	v_mfma_scale_f32_16x16x128_f8f6f4 v[92:95], v[16:23], v[186:193], 0, v200, v201 op_sel_hi:[0,0,0]
	v_mfma_scale_f32_16x16x128_f8f6f4 v[88:91], v[24:31], v[186:193], 0, v200, v201 op_sel_hi:[0,0,0]
	v_mfma_scale_f32_16x16x128_f8f6f4 v[76:79], v[16:23], v[206:213], 0, v200, v201 op_sel_hi:[0,0,0]
	v_mfma_scale_f32_16x16x128_f8f6f4 v[72:75], v[24:31], v[206:213], 0, v200, v201 op_sel_hi:[0,0,0]
	v_mfma_scale_f32_16x16x128_f8f6f4 v[60:63], v[16:23], v[216:223], 0, v200, v201 op_sel_hi:[0,0,0]
	v_mfma_scale_f32_16x16x128_f8f6f4 v[56:59], v[24:31], v[216:223], 0, v200, v201 op_sel_hi:[0,0,0]
	v_mfma_scale_f32_16x16x128_f8f6f4 v[44:47], v[16:23], v[224:231], 0, v200, v201 op_sel_hi:[0,0,0]
	v_mfma_scale_f32_16x16x128_f8f6f4 v[40:43], v[24:31], v[224:231], 0, v200, v201 op_sel_hi:[0,0,0]
	s_setprio 0
	s_setprio 1
	v_mfma_scale_f32_16x16x128_f8f6f4 v[84:87], v[0:7], v[186:193], 0, v200, v201 op_sel_hi:[0,0,0]
	v_mfma_scale_f32_16x16x128_f8f6f4 v[80:83], v[8:15], v[186:193], 0, v200, v201 op_sel_hi:[0,0,0]
	v_mfma_scale_f32_16x16x128_f8f6f4 v[68:71], v[0:7], v[206:213], 0, v200, v201 op_sel_hi:[0,0,0]
	v_mfma_scale_f32_16x16x128_f8f6f4 v[64:67], v[8:15], v[206:213], 0, v200, v201 op_sel_hi:[0,0,0]
	v_mfma_scale_f32_16x16x128_f8f6f4 v[52:55], v[0:7], v[216:223], 0, v200, v201 op_sel_hi:[0,0,0]
	v_mfma_scale_f32_16x16x128_f8f6f4 v[48:51], v[8:15], v[216:223], 0, v200, v201 op_sel_hi:[0,0,0]
	v_mfma_scale_f32_16x16x128_f8f6f4 v[36:39], v[0:7], v[224:231], 0, v200, v201 op_sel_hi:[0,0,0]
	v_mfma_scale_f32_16x16x128_f8f6f4 v[32:35], v[8:15], v[224:231], 0, v200, v201 op_sel_hi:[0,0,0]
	s_setprio 0
	s_barrier
	s_add_i32 s45, 0, 0x18000
	s_add_i32 s51, 0, 0x1c000
	v_add_u32_e32 v12, s45, v183
	v_add_u32_e32 v28, s51, v183
	ds_read_b128 v[0:3], v12
	ds_read_b128 v[4:7], v12 offset:1024
	ds_read_b128 v[8:11], v12 offset:2048
	ds_read_b128 v[12:15], v12 offset:3072
	ds_read_b128 v[16:19], v28
	ds_read_b128 v[20:23], v28 offset:1024
	ds_read_b128 v[24:27], v28 offset:2048
	ds_read_b128 v[28:31], v28 offset:3072
	s_add_u32 s30, s76, 0x20000
	s_addc_u32 s31, s77, 0
	s_mov_b32 m0, s33
	v_lshl_add_u64 v[194:195], s[30:31], 0, v[166:167]
	ds_read_b128 v[186:189], v184 offset:32768
	ds_read_b128 v[190:193], v184 offset:33792
	ds_read_b128 v[206:209], v184 offset:34816
	ds_read_b128 v[210:213], v184 offset:35840
	ds_read_b128 v[216:219], v184 offset:36864
	ds_read_b128 v[220:223], v184 offset:37888
	ds_read_b128 v[224:227], v184 offset:38912
	ds_read_b128 v[228:231], v184 offset:39936
	global_load_lds_dwordx4 v[194:195], off
	v_lshl_add_u64 v[194:195], s[30:31], 0, v[164:165]
	s_mov_b32 m0, s34
	s_nop 0
	global_load_lds_dwordx4 v[194:195], off
	s_waitcnt vmcnt(8)
	s_waitcnt lgkmcnt(0)
	s_barrier
	s_setprio 1
	s_waitcnt lgkmcnt(0)
	v_mfma_scale_f32_16x16x128_f8f6f4 v[158:161], v[0:7], v[186:193], v[158:161], v200, v201 op_sel_hi:[0,0,0]
	v_mfma_scale_f32_16x16x128_f8f6f4 v[154:157], v[8:15], v[186:193], v[154:157], v200, v201 op_sel_hi:[0,0,0]
	v_mfma_scale_f32_16x16x128_f8f6f4 v[142:145], v[0:7], v[206:213], v[142:145], v200, v201 op_sel_hi:[0,0,0]
	v_mfma_scale_f32_16x16x128_f8f6f4 v[138:141], v[8:15], v[206:213], v[138:141], v200, v201 op_sel_hi:[0,0,0]
	v_mfma_scale_f32_16x16x128_f8f6f4 v[126:129], v[0:7], v[216:223], v[126:129], v200, v201 op_sel_hi:[0,0,0]
	v_mfma_scale_f32_16x16x128_f8f6f4 v[122:125], v[8:15], v[216:223], v[122:125], v200, v201 op_sel_hi:[0,0,0]
	v_mfma_scale_f32_16x16x128_f8f6f4 v[108:111], v[0:7], v[224:231], v[108:111], v200, v201 op_sel_hi:[0,0,0]
	v_mfma_scale_f32_16x16x128_f8f6f4 v[104:107], v[8:15], v[224:231], v[104:107], v200, v201 op_sel_hi:[0,0,0]
	s_setprio 0
	s_setprio 1
	v_mfma_scale_f32_16x16x128_f8f6f4 v[150:153], v[16:23], v[186:193], v[150:153], v200, v201 op_sel_hi:[0,0,0]
	v_mfma_scale_f32_16x16x128_f8f6f4 v[146:149], v[24:31], v[186:193], v[146:149], v200, v201 op_sel_hi:[0,0,0]
	v_mfma_scale_f32_16x16x128_f8f6f4 v[134:137], v[16:23], v[206:213], v[134:137], v200, v201 op_sel_hi:[0,0,0]
	v_mfma_scale_f32_16x16x128_f8f6f4 v[130:133], v[24:31], v[206:213], v[130:133], v200, v201 op_sel_hi:[0,0,0]
	v_mfma_scale_f32_16x16x128_f8f6f4 v[118:121], v[16:23], v[216:223], v[118:121], v200, v201 op_sel_hi:[0,0,0]
	v_mfma_scale_f32_16x16x128_f8f6f4 v[114:117], v[24:31], v[216:223], v[114:117], v200, v201 op_sel_hi:[0,0,0]
	v_mfma_scale_f32_16x16x128_f8f6f4 v[100:103], v[16:23], v[224:231], v[100:103], v200, v201 op_sel_hi:[0,0,0]
	v_mfma_scale_f32_16x16x128_f8f6f4 v[96:99], v[24:31], v[224:231], v[96:99], v200, v201 op_sel_hi:[0,0,0]
	s_setprio 0
	s_barrier
	s_add_i32 s30, s45, s14
	v_lshl_add_u64 v[174:175], v[174:175], 0, s[56:57]
	s_mov_b32 m0, s30
	ds_read_b128 v[186:189], v184 offset:49152
	ds_read_b128 v[190:193], v184 offset:50176
	ds_read_b128 v[206:209], v184 offset:51200
	ds_read_b128 v[210:213], v184 offset:52224
	ds_read_b128 v[216:219], v184 offset:53248
	ds_read_b128 v[220:223], v184 offset:54272
	ds_read_b128 v[224:227], v184 offset:55296
	ds_read_b128 v[228:231], v184 offset:56320
	global_load_lds_dwordx4 v[174:175], off
	s_add_i32 m0, s30, 0x2000
	s_add_u32 s30, s74, 0x20080
	v_lshl_add_u64 v[174:175], v[176:177], 0, s[56:57]
	s_addc_u32 s31, s75, 0
	s_add_i32 s45, s51, s14
	global_load_lds_dwordx4 v[174:175], off
	v_lshl_add_u64 v[174:175], s[30:31], 0, v[112:113]
	s_mov_b32 m0, s45
	s_nop 0
	global_load_lds_dwordx4 v[174:175], off
	v_lshl_add_u64 v[174:175], s[30:31], 0, v[162:163]
	s_add_i32 m0, s45, 0x2000
	s_nop 0
	global_load_lds_dwordx4 v[174:175], off
	v_lshl_add_u64 v[174:175], v[178:179], 0, s[56:57]
	s_mov_b32 m0, s4
	s_nop 0
	global_load_lds_dwordx4 v[174:175], off
	v_lshl_add_u64 v[174:175], v[180:181], 0, s[56:57]
	s_mov_b32 m0, s54
	s_nop 0
	global_load_lds_dwordx4 v[174:175], off
	s_waitcnt vmcnt(8)
	s_waitcnt lgkmcnt(0)
	s_barrier
	s_setprio 1
	s_waitcnt lgkmcnt(0)
	v_mfma_scale_f32_16x16x128_f8f6f4 v[92:95], v[0:7], v[186:193], v[92:95], v200, v201 op_sel_hi:[0,0,0]
	v_mfma_scale_f32_16x16x128_f8f6f4 v[88:91], v[8:15], v[186:193], v[88:91], v200, v201 op_sel_hi:[0,0,0]
	v_mfma_scale_f32_16x16x128_f8f6f4 v[76:79], v[0:7], v[206:213], v[76:79], v200, v201 op_sel_hi:[0,0,0]
	v_mfma_scale_f32_16x16x128_f8f6f4 v[72:75], v[8:15], v[206:213], v[72:75], v200, v201 op_sel_hi:[0,0,0]
	v_mfma_scale_f32_16x16x128_f8f6f4 v[60:63], v[0:7], v[216:223], v[60:63], v200, v201 op_sel_hi:[0,0,0]
	v_mfma_scale_f32_16x16x128_f8f6f4 v[56:59], v[8:15], v[216:223], v[56:59], v200, v201 op_sel_hi:[0,0,0]
	v_mfma_scale_f32_16x16x128_f8f6f4 v[44:47], v[0:7], v[224:231], v[44:47], v200, v201 op_sel_hi:[0,0,0]
	v_mfma_scale_f32_16x16x128_f8f6f4 v[40:43], v[8:15], v[224:231], v[40:43], v200, v201 op_sel_hi:[0,0,0]
	s_setprio 0
	s_setprio 1
	v_mfma_scale_f32_16x16x128_f8f6f4 v[84:87], v[16:23], v[186:193], v[84:87], v200, v201 op_sel_hi:[0,0,0]
	v_mfma_scale_f32_16x16x128_f8f6f4 v[80:83], v[24:31], v[186:193], v[80:83], v200, v201 op_sel_hi:[0,0,0]
	v_mfma_scale_f32_16x16x128_f8f6f4 v[68:71], v[16:23], v[206:213], v[68:71], v200, v201 op_sel_hi:[0,0,0]
	v_mfma_scale_f32_16x16x128_f8f6f4 v[64:67], v[24:31], v[206:213], v[64:67], v200, v201 op_sel_hi:[0,0,0]
	v_mfma_scale_f32_16x16x128_f8f6f4 v[52:55], v[16:23], v[216:223], v[52:55], v200, v201 op_sel_hi:[0,0,0]
	v_mfma_scale_f32_16x16x128_f8f6f4 v[48:51], v[24:31], v[216:223], v[48:51], v200, v201 op_sel_hi:[0,0,0]
	v_mfma_scale_f32_16x16x128_f8f6f4 v[36:39], v[16:23], v[224:231], v[36:39], v200, v201 op_sel_hi:[0,0,0]
	v_mfma_scale_f32_16x16x128_f8f6f4 v[32:35], v[24:31], v[224:231], v[32:35], v200, v201 op_sel_hi:[0,0,0]
	s_setprio 0
	s_barrier
	s_add_i32 s50, s50, 2
	s_add_u32 s72, s72, 0x100
	s_addc_u32 s73, s73, 0
	s_add_u32 s47, s47, 0x100
	s_addc_u32 s49, s49, 0
	s_cmp_gt_u32 s50, 5
	.p2align	6
